# peer_gather transposing butterfly: xor-32 and xor-16 exchange rounds via v_permlane32/16_swap instead of cndmask pair + ds_bpermute
# speedup vs baseline: 1.0268x; 1.0093x over previous
.LBB0_763:
	s_cmpk_eq_i32 s58, 0x80
	s_cselect_b64 s[12:13], -1, 0
	ds_bpermute_b32 v84, v93, v92
	s_and_b64 vcc, s[12:13], s[48:49]
	v_cndmask_b32_e32 v104, v0, v94, vcc
	v_ashrrev_i32_e32 v105, 31, v104
	s_and_b32 s12, s58, 0x70
	v_lshlrev_b64 v[104:105], 9, v[104:105]
	v_lshl_add_u64 v[104:105], s[94:95], 0, v[104:105]
	s_lshl_b32 s36, s12, 2
	s_waitcnt lgkmcnt(0)
	v_ashrrev_i32_e32 v85, 31, v84
	v_lshl_add_u64 v[104:105], v[104:105], 0, s[36:37]
	v_lshl_add_u64 v[84:85], v[84:85], 3, s[8:9]
	v_lshl_add_u64 v[104:105], v[104:105], 0, v[144:145]
	global_load_dwordx2 v[84:85], v[84:85], off
	s_nop 0
	global_load_dword v86, v[72:73], off
	global_load_dword v92, v[104:105], off
	s_waitcnt vmcnt(11)
	v_dot8_i32_i4 v87, v8, v1, 0
	v_dot8_i32_i4 v104, v8, v88, 0
	v_dot8_i32_i4 v87, v9, v89, v87
	v_dot8_i32_i4 v104, v9, v90, v104
	s_waitcnt vmcnt(10)
	v_dot8_i32_i4 v9, v10, v88, 0
	v_dot8_i32_i4 v9, v11, v90, v9
	v_lshl_add_u32 v8, v87, 4, v104
	v_cvt_f32_i32_e32 v87, v8
	v_dot8_i32_i4 v8, v10, v1, 0
	v_dot8_i32_i4 v8, v11, v89, v8
	s_add_i32 s58, s58, 16
	v_lshl_add_u64 v[72:73], v[72:73], 0, 64
	s_waitcnt vmcnt(2)
	v_mul_f32_e32 v85, v91, v85
	v_lshl_add_u32 v8, v8, 4, v9
	v_cvt_f32_i32_e32 v104, v8
	v_dot8_i32_i4 v8, v12, v1, 0
	v_dot8_i32_i4 v9, v12, v88, 0
	v_dot8_i32_i4 v8, v13, v89, v8
	v_dot8_i32_i4 v9, v13, v90, v9
	s_waitcnt vmcnt(0)
	v_readlane_b32 s12, v92, 0
	v_readlane_b32 s28, v92, 8
	v_readlane_b32 s30, v92, 9
	v_lshl_add_u32 v8, v8, 4, v9
	v_cvt_f32_i32_e32 v105, v8
	v_dot8_i32_i4 v8, v14, v1, 0
	v_dot8_i32_i4 v9, v14, v88, 0
	v_dot8_i32_i4 v8, v15, v89, v8
	v_dot8_i32_i4 v9, v15, v90, v9
	s_ashr_i32 s13, s12, 31
	v_readlane_b32 s14, v92, 1
	s_ashr_i32 s29, s28, 31
	v_lshl_add_u32 v8, v8, 4, v9
	v_cvt_f32_i32_e32 v106, v8
	v_dot8_i32_i4 v8, v16, v1, 0
	v_dot8_i32_i4 v9, v16, v88, 0
	v_dot8_i32_i4 v8, v17, v89, v8
	v_dot8_i32_i4 v9, v17, v90, v9
	s_ashr_i32 s31, s30, 31
	v_readlane_b32 s34, v92, 10
	s_lshl_b64 s[12:13], s[12:13], 9
	v_lshl_add_u32 v8, v8, 4, v9
	v_cvt_f32_i32_e32 v107, v8
	v_dot8_i32_i4 v8, v18, v1, 0
	v_dot8_i32_i4 v9, v18, v88, 0
	v_dot8_i32_i4 v8, v19, v89, v8
	v_dot8_i32_i4 v9, v19, v90, v9
	s_ashr_i32 s15, s14, 31
	v_readlane_b32 s16, v92, 2
	s_lshl_b64 s[28:29], s[28:29], 9
	v_lshl_add_u32 v8, v8, 4, v9
	v_cvt_f32_i32_e32 v108, v8
	v_dot8_i32_i4 v8, v20, v1, 0
	v_dot8_i32_i4 v9, v20, v88, 0
	v_dot8_i32_i4 v8, v21, v89, v8
	v_dot8_i32_i4 v9, v21, v90, v9
	s_lshl_b64 s[30:31], s[30:31], 9
	s_ashr_i32 s35, s34, 31
	v_readlane_b32 s38, v92, 11
	v_lshl_add_u32 v8, v8, 4, v9
	v_cvt_f32_i32_e32 v109, v8
	v_dot8_i32_i4 v8, v22, v1, 0
	v_dot8_i32_i4 v9, v22, v88, 0
	v_dot8_i32_i4 v8, v23, v89, v8
	v_dot8_i32_i4 v9, v23, v90, v9
	s_lshl_b64 s[14:15], s[14:15], 9
	s_ashr_i32 s17, s16, 31
	v_readlane_b32 s18, v92, 3
	v_lshl_add_u32 v8, v8, 4, v9
	v_cvt_f32_i32_e32 v110, v8
	v_dot8_i32_i4 v8, v24, v1, 0
	v_dot8_i32_i4 v9, v24, v88, 0
	v_dot8_i32_i4 v8, v25, v89, v8
	v_dot8_i32_i4 v9, v25, v90, v9
	v_lshl_add_u64 v[24:25], v[4:5], 0, s[28:29]
	s_lshl_b64 s[34:35], s[34:35], 9
	s_ashr_i32 s39, s38, 31
	v_lshl_add_u32 v8, v8, 4, v9
	v_cvt_f32_i32_e32 v111, v8
	v_dot8_i32_i4 v8, v38, v1, 0
	v_dot8_i32_i4 v9, v38, v88, 0
	v_dot8_i32_i4 v8, v39, v89, v8
	v_dot8_i32_i4 v9, v39, v90, v9
	v_permlane32_swap_b32 v87, v111
	s_nop 1
	v_lshl_add_u32 v8, v8, 4, v9
	v_cvt_f32_i32_e32 v112, v8
	v_dot8_i32_i4 v8, v50, v1, 0
	v_dot8_i32_i4 v9, v50, v88, 0
	v_dot8_i32_i4 v8, v51, v89, v8
	v_dot8_i32_i4 v9, v51, v90, v9
	s_waitcnt lgkmcnt(0)
	v_add_f32_e32 v87, v87, v111
	v_permlane32_swap_b32 v104, v112
	v_lshl_add_u32 v8, v8, 4, v9
	v_cvt_f32_i32_e32 v113, v8
	v_dot8_i32_i4 v8, v48, v1, 0
	v_dot8_i32_i4 v9, v48, v88, 0
	v_dot8_i32_i4 v8, v49, v89, v8
	v_dot8_i32_i4 v9, v49, v90, v9
	s_waitcnt lgkmcnt(0)
	v_add_f32_e32 v104, v104, v112
	v_permlane32_swap_b32 v105, v113
	v_lshl_add_u32 v8, v8, 4, v9
	v_cvt_f32_i32_e32 v114, v8
	v_dot8_i32_i4 v8, v46, v1, 0
	v_dot8_i32_i4 v9, v46, v88, 0
	v_dot8_i32_i4 v8, v47, v89, v8
	v_dot8_i32_i4 v9, v47, v90, v9
	s_waitcnt lgkmcnt(0)
	v_add_f32_e32 v105, v105, v113
	v_permlane32_swap_b32 v106, v114
	v_lshl_add_u32 v8, v8, 4, v9
	v_cvt_f32_i32_e32 v115, v8
	v_dot8_i32_i4 v8, v44, v1, 0
	v_dot8_i32_i4 v9, v44, v88, 0
	v_dot8_i32_i4 v8, v45, v89, v8
	v_dot8_i32_i4 v9, v45, v90, v9
	s_waitcnt lgkmcnt(0)
	v_add_f32_e32 v106, v106, v114
	v_permlane32_swap_b32 v107, v115
	v_lshl_add_u32 v8, v8, 4, v9
	v_cvt_f32_i32_e32 v116, v8
	v_dot8_i32_i4 v8, v42, v1, 0
	v_dot8_i32_i4 v9, v42, v88, 0
	v_dot8_i32_i4 v8, v43, v89, v8
	v_dot8_i32_i4 v9, v43, v90, v9
	s_waitcnt lgkmcnt(0)
	v_add_f32_e32 v107, v107, v115
	v_permlane32_swap_b32 v108, v116
	v_lshl_add_u32 v8, v8, 4, v9
	v_cvt_f32_i32_e32 v117, v8
	v_dot8_i32_i4 v8, v40, v1, 0
	v_dot8_i32_i4 v9, v40, v88, 0
	v_dot8_i32_i4 v8, v41, v89, v8
	v_dot8_i32_i4 v9, v41, v90, v9
	s_waitcnt lgkmcnt(0)
	v_add_f32_e32 v108, v108, v116
	v_permlane32_swap_b32 v109, v117
	v_lshl_add_u32 v8, v8, 4, v9
	v_cvt_f32_i32_e32 v118, v8
	v_lshl_add_u64 v[38:39], v[4:5], 0, s[30:31]
	s_waitcnt lgkmcnt(0)
	v_add_f32_e32 v109, v109, v117
	v_permlane32_swap_b32 v110, v118
	v_readlane_b32 s50, v92, 12
	s_lshl_b64 s[16:17], s[16:17], 9
	s_ashr_i32 s19, s18, 31
	s_waitcnt lgkmcnt(0)
	v_add_f32_e32 v110, v110, v118
	v_permlane16_swap_b32 v87, v107
	v_readlane_b32 s20, v92, 4
	global_load_dwordx2 v[24:25], v[24:25], off
	v_lshl_add_u64 v[40:41], v[4:5], 0, s[34:35]
	global_load_dwordx2 v[38:39], v[38:39], off
	s_waitcnt lgkmcnt(0)
	v_add_f32_e32 v87, v87, v107
	v_permlane16_swap_b32 v104, v108
	s_lshl_b64 s[38:39], s[38:39], 9
	s_ashr_i32 s51, s50, 31
	v_readlane_b32 s52, v92, 13
	s_waitcnt lgkmcnt(0)
	v_add_f32_e32 v104, v104, v108
	v_permlane16_swap_b32 v105, v109
	s_lshl_b64 s[18:19], s[18:19], 9
	s_ashr_i32 s21, s20, 31
	v_readlane_b32 s22, v92, 5
	s_waitcnt lgkmcnt(0)
	v_add_f32_e32 v105, v105, v109
	v_permlane16_swap_b32 v106, v110
	global_load_dwordx2 v[50:51], v[40:41], off
	s_lshl_b64 s[50:51], s[50:51], 9
	s_ashr_i32 s53, s52, 31
	s_waitcnt lgkmcnt(0)
	v_add_f32_e32 v106, v106, v110
	v_cndmask_b32_e64 v107, v87, v105, s[44:45]
	v_cndmask_b32_e64 v87, v105, v87, s[44:45]
	ds_bpermute_b32 v105, v186, v107
	v_readlane_b32 s54, v92, 14
	s_lshl_b64 s[20:21], s[20:21], 9
	s_ashr_i32 s23, s22, 31
	v_readlane_b32 s24, v92, 6
	s_waitcnt lgkmcnt(0)
	v_add_f32_e32 v87, v87, v105
	v_cndmask_b32_e64 v105, v104, v106, s[44:45]
	ds_bpermute_b32 v105, v186, v105
	v_cndmask_b32_e64 v104, v106, v104, s[44:45]
	s_lshl_b64 s[52:53], s[52:53], 9
	s_ashr_i32 s55, s54, 31
	v_readlane_b32 s56, v92, 15
	s_waitcnt lgkmcnt(0)
	v_add_f32_e32 v104, v104, v105
	v_cndmask_b32_e64 v105, v87, v104, s[46:47]
	v_cndmask_b32_e64 v87, v104, v87, s[46:47]
	ds_bpermute_b32 v104, v187, v105
	s_lshl_b64 s[22:23], s[22:23], 9
	s_ashr_i32 s25, s24, 31
	v_readlane_b32 s26, v92, 7
	s_lshl_b64 s[54:55], s[54:55], 9
	s_waitcnt lgkmcnt(0)
	v_add_f32_e32 v87, v87, v104
	ds_bpermute_b32 v104, v188, v87
	s_ashr_i32 s57, s56, 31
	s_lshl_b64 s[24:25], s[24:25], 9
	s_ashr_i32 s27, s26, 31
	s_lshl_b64 s[56:57], s[56:57], 9
	s_waitcnt lgkmcnt(0)
	v_add_f32_e32 v87, v87, v104
	ds_bpermute_b32 v104, v189, v87
	s_lshl_b64 s[26:27], s[26:27], 9
	v_lshl_add_u64 v[8:9], v[4:5], 0, s[12:13]
	v_lshl_add_u64 v[10:11], v[4:5], 0, s[14:15]
	v_lshl_add_u64 v[12:13], v[4:5], 0, s[16:17]
	s_waitcnt lgkmcnt(0)
	v_add_f32_e32 v87, v87, v104
	v_add_f32_e32 v87, v95, v87
	v_mul_f32_e32 v85, v85, v87
	v_mul_f32_e32 v87, 0x3d372713, v85
	v_mul_f32_e32 v87, v85, v87
	v_fma_f32 v87, v85, v87, v85
	v_mul_f32_e32 v87, 0x3fcc422a, v87
	v_mul_f32_e32 v87, 0xbfb8aa3b, v87
	v_exp_f32_e32 v87, v87
	v_lshlrev_b32_e32 v104, 4, v82
	v_lshl_add_u64 v[14:15], v[4:5], 0, s[18:19]
	v_lshl_add_u64 v[16:17], v[4:5], 0, s[20:21]
	v_add_f32_e32 v87, 1.0, v87
	v_rcp_f32_e32 v87, v87
	v_lshl_add_u64 v[18:19], v[4:5], 0, s[22:23]
	v_lshl_add_u64 v[20:21], v[4:5], 0, s[24:25]
	v_lshl_add_u64 v[22:23], v[4:5], 0, s[26:27]
	v_pk_mul_f32 v[84:85], v[84:85], v[86:87]
	v_lshrrev_b32_e32 v87, 4, v82
	v_pk_mul_f32 v[84:85], v[84:85], v[84:85] op_sel:[0,1] op_sel_hi:[1,0]
	v_cvt_f16_f32_e32 v120, v84
	v_and_b32_e32 v86, 0x7070707, v82
	v_readlane_b32 s36, v120, 0
	v_and_b32_e32 v87, 0x7070707, v87
	v_perm_b32 v86, s2, v205, v86
	v_perm_b32 v87, s2, v205, v87
	v_and_or_b32 v86, v104, s4, v86
	v_and_or_b32 v82, v82, s4, v87
	v_perm_b32 v87, v82, v86, s5
	v_perm_b32 v104, v82, v86, s33
	v_perm_b32 v105, v82, v86, s0
	v_perm_b32 v82, v82, v86, s1
	v_pk_fma_f16 v86, v87, s36, v103 op_sel_hi:[1,0,1]
	v_pk_fma_f16 v87, v104, s36, v102 op_sel_hi:[1,0,1]
	v_lshrrev_b32_e32 v102, 4, v83
	v_pk_fma_f16 v82, v82, s36, v100 op_sel_hi:[1,0,1]
	v_and_b32_e32 v100, 0x7070707, v83
	v_and_b32_e32 v102, 0x7070707, v102
	v_perm_b32 v100, s2, v205, v100
	v_perm_b32 v102, s2, v205, v102
	v_lshlrev_b32_e32 v103, 4, v83
	v_and_or_b32 v100, v103, s4, v100
	v_and_or_b32 v83, v83, s4, v102
	v_perm_b32 v102, v83, v100, s5
	v_perm_b32 v103, v83, v100, s33
	v_perm_b32 v104, v83, v100, s0
	v_perm_b32 v83, v83, v100, s1
	v_readlane_b32 s59, v120, 4
	v_lshrrev_b32_e32 v100, 4, v80
	v_pk_fma_f16 v101, v105, s36, v101 op_sel_hi:[1,0,1]
	v_pk_fma_f16 v99, v102, s36, v99 op_sel_hi:[1,0,1]
	v_pk_fma_f16 v98, v103, s36, v98 op_sel_hi:[1,0,1]
	v_pk_fma_f16 v97, v104, s36, v97 op_sel_hi:[1,0,1]
	v_pk_fma_f16 v83, v83, s36, v96 op_sel_hi:[1,0,1]
	v_and_b32_e32 v96, 0x7070707, v80
	v_and_b32_e32 v100, 0x7070707, v100
	v_perm_b32 v96, s2, v205, v96
	v_perm_b32 v100, s2, v205, v100
	v_lshlrev_b32_e32 v102, 4, v80
	v_and_or_b32 v96, v102, s4, v96
	v_and_or_b32 v80, v80, s4, v100
	v_perm_b32 v100, v80, v96, s5
	v_perm_b32 v102, v80, v96, s33
	v_perm_b32 v103, v80, v96, s0
	v_perm_b32 v80, v80, v96, s1
	v_pk_fma_f16 v86, v100, s59, v86 op_sel_hi:[1,0,1]
	v_lshrrev_b32_e32 v100, 4, v81
	v_pk_fma_f16 v80, v80, s59, v82 op_sel_hi:[1,0,1]
	v_and_b32_e32 v82, 0x7070707, v81
	v_and_b32_e32 v100, 0x7070707, v100
	v_pk_fma_f16 v96, v103, s59, v101 op_sel_hi:[1,0,1]
	v_perm_b32 v82, s2, v205, v82
	v_perm_b32 v100, s2, v205, v100
	v_lshlrev_b32_e32 v101, 4, v81
	v_and_or_b32 v82, v101, s4, v82
	v_and_or_b32 v81, v81, s4, v100
	v_perm_b32 v100, v81, v82, s5
	v_pk_fma_f16 v87, v102, s59, v87 op_sel_hi:[1,0,1]
	v_perm_b32 v101, v81, v82, s33
	v_perm_b32 v102, v81, v82, s0
	v_perm_b32 v81, v81, v82, s1
	v_pk_fma_f16 v82, v100, s59, v99 op_sel_hi:[1,0,1]
	v_readlane_b32 s60, v120, 8
	v_lshrrev_b32_e32 v99, 4, v78
	v_pk_fma_f16 v98, v101, s59, v98 op_sel_hi:[1,0,1]
	v_pk_fma_f16 v97, v102, s59, v97 op_sel_hi:[1,0,1]
	v_pk_fma_f16 v81, v81, s59, v83 op_sel_hi:[1,0,1]
	v_and_b32_e32 v85, 0x7070707, v78
	v_and_b32_e32 v99, 0x7070707, v99
	v_perm_b32 v85, s2, v205, v85
	v_perm_b32 v99, s2, v205, v99
	v_lshlrev_b32_e32 v100, 4, v78
	v_and_or_b32 v85, v100, s4, v85
	v_and_or_b32 v78, v78, s4, v99
	v_perm_b32 v99, v78, v85, s5
	v_perm_b32 v100, v78, v85, s33
	v_perm_b32 v101, v78, v85, s0
	v_perm_b32 v78, v78, v85, s1
	v_pk_fma_f16 v85, v99, s60, v86 op_sel_hi:[1,0,1]
	v_pk_fma_f16 v86, v100, s60, v87 op_sel_hi:[1,0,1]
	v_pk_fma_f16 v87, v101, s60, v96 op_sel_hi:[1,0,1]
	v_lshrrev_b32_e32 v96, 4, v79
	v_pk_fma_f16 v78, v78, s60, v80 op_sel_hi:[1,0,1]
	v_and_b32_e32 v80, 0x7070707, v79
	v_and_b32_e32 v96, 0x7070707, v96
	v_perm_b32 v80, s2, v205, v80
	v_perm_b32 v96, s2, v205, v96
	v_lshlrev_b32_e32 v99, 4, v79
	v_and_or_b32 v80, v99, s4, v80
	v_and_or_b32 v79, v79, s4, v96
	v_perm_b32 v96, v79, v80, s5
	v_perm_b32 v100, v79, v80, s0
	v_perm_b32 v99, v79, v80, s33
	v_perm_b32 v79, v79, v80, s1
	v_pk_fma_f16 v80, v96, s60, v82 op_sel_hi:[1,0,1]
	v_pk_fma_f16 v96, v100, s60, v97 op_sel_hi:[1,0,1]
	v_readlane_b32 s36, v120, 12
	v_lshrrev_b32_e32 v97, 4, v76
	v_pk_fma_f16 v82, v99, s60, v98 op_sel_hi:[1,0,1]
	v_pk_fma_f16 v79, v79, s60, v81 op_sel_hi:[1,0,1]
	v_and_b32_e32 v83, 0x7070707, v76
	v_and_b32_e32 v97, 0x7070707, v97
	v_perm_b32 v83, s2, v205, v83
	v_perm_b32 v97, s2, v205, v97
	v_lshlrev_b32_e32 v98, 4, v76
	v_and_or_b32 v83, v98, s4, v83
	v_and_or_b32 v76, v76, s4, v97
	v_perm_b32 v97, v76, v83, s5
	v_perm_b32 v98, v76, v83, s33
	v_perm_b32 v99, v76, v83, s0
	v_perm_b32 v76, v76, v83, s1
	v_pk_fma_f16 v83, v97, s36, v85 op_sel_hi:[1,0,1]
	v_pk_fma_f16 v85, v98, s36, v86 op_sel_hi:[1,0,1]
	v_pk_fma_f16 v86, v99, s36, v87 op_sel_hi:[1,0,1]
	v_lshrrev_b32_e32 v87, 4, v77
	v_pk_fma_f16 v76, v76, s36, v78 op_sel_hi:[1,0,1]
	v_and_b32_e32 v78, 0x7070707, v77
	v_and_b32_e32 v87, 0x7070707, v87
	v_perm_b32 v78, s2, v205, v78
	v_perm_b32 v87, s2, v205, v87
	v_lshlrev_b32_e32 v97, 4, v77
	v_and_or_b32 v78, v97, s4, v78
	v_and_or_b32 v77, v77, s4, v87
	v_perm_b32 v87, v77, v78, s5
	v_perm_b32 v97, v77, v78, s33
	v_perm_b32 v98, v77, v78, s0
	v_perm_b32 v77, v77, v78, s1
	v_pk_fma_f16 v78, v87, s36, v80 op_sel_hi:[1,0,1]
	v_readlane_b32 s59, v120, 16
	v_lshrrev_b32_e32 v87, 4, v74
	v_pk_fma_f16 v80, v97, s36, v82 op_sel_hi:[1,0,1]
	v_pk_fma_f16 v82, v98, s36, v96 op_sel_hi:[1,0,1]
	v_pk_fma_f16 v77, v77, s36, v79 op_sel_hi:[1,0,1]
	v_and_b32_e32 v81, 0x7070707, v74
	v_and_b32_e32 v87, 0x7070707, v87
	v_perm_b32 v81, s2, v205, v81
	v_perm_b32 v87, s2, v205, v87
	v_lshlrev_b32_e32 v96, 4, v74
	v_and_or_b32 v81, v96, s4, v81
	v_and_or_b32 v74, v74, s4, v87
	v_perm_b32 v87, v74, v81, s5
	v_perm_b32 v96, v74, v81, s33
	v_perm_b32 v97, v74, v81, s0
	v_perm_b32 v74, v74, v81, s1
	v_pk_fma_f16 v81, v87, s59, v83 op_sel_hi:[1,0,1]
	v_pk_fma_f16 v83, v96, s59, v85 op_sel_hi:[1,0,1]
	v_pk_fma_f16 v85, v97, s59, v86 op_sel_hi:[1,0,1]
	v_lshrrev_b32_e32 v86, 4, v75
	v_pk_fma_f16 v74, v74, s59, v76 op_sel_hi:[1,0,1]
	v_and_b32_e32 v76, 0x7070707, v75
	v_and_b32_e32 v86, 0x7070707, v86
	v_perm_b32 v76, s2, v205, v76
	v_perm_b32 v86, s2, v205, v86
	v_lshlrev_b32_e32 v87, 4, v75
	v_and_or_b32 v76, v87, s4, v76
	v_and_or_b32 v75, v75, s4, v86
	v_perm_b32 v86, v75, v76, s5
	v_perm_b32 v87, v75, v76, s33
	v_perm_b32 v96, v75, v76, s0
	v_perm_b32 v75, v75, v76, s1
	v_pk_fma_f16 v76, v86, s59, v78 op_sel_hi:[1,0,1]
	v_pk_fma_f16 v78, v87, s59, v80 op_sel_hi:[1,0,1]
	v_pk_fma_f16 v80, v96, s59, v82 op_sel_hi:[1,0,1]
	v_readlane_b32 s60, v120, 20
	v_lshrrev_b32_e32 v82, 4, v70
	v_pk_fma_f16 v75, v75, s59, v77 op_sel_hi:[1,0,1]
	v_and_b32_e32 v79, 0x7070707, v70
	v_and_b32_e32 v82, 0x7070707, v82
	v_perm_b32 v79, s2, v205, v79
	v_perm_b32 v82, s2, v205, v82
	v_lshlrev_b32_e32 v86, 4, v70
	v_and_or_b32 v79, v86, s4, v79
	v_and_or_b32 v70, v70, s4, v82
	v_perm_b32 v82, v70, v79, s5
	v_perm_b32 v86, v70, v79, s33
	v_perm_b32 v87, v70, v79, s0
	v_perm_b32 v70, v70, v79, s1
	v_pk_fma_f16 v79, v82, s60, v81 op_sel_hi:[1,0,1]
	v_pk_fma_f16 v81, v86, s60, v83 op_sel_hi:[1,0,1]
	v_lshrrev_b32_e32 v83, 4, v71
	v_pk_fma_f16 v70, v70, s60, v74 op_sel_hi:[1,0,1]
	v_and_b32_e32 v74, 0x7070707, v71
	v_and_b32_e32 v83, 0x7070707, v83
	v_pk_fma_f16 v82, v87, s60, v85 op_sel_hi:[1,0,1]
	v_perm_b32 v74, s2, v205, v74
	v_perm_b32 v83, s2, v205, v83
	v_lshlrev_b32_e32 v85, 4, v71
	v_and_or_b32 v74, v85, s4, v74
	v_and_or_b32 v71, v71, s4, v83
	v_perm_b32 v83, v71, v74, s5
	v_perm_b32 v85, v71, v74, s33
	v_perm_b32 v86, v71, v74, s0
	v_perm_b32 v71, v71, v74, s1
	v_pk_fma_f16 v74, v83, s60, v76 op_sel_hi:[1,0,1]
	v_pk_fma_f16 v76, v85, s60, v78 op_sel_hi:[1,0,1]
	v_pk_fma_f16 v78, v86, s60, v80 op_sel_hi:[1,0,1]
	v_readlane_b32 s36, v120, 24
	v_lshrrev_b32_e32 v80, 4, v68
	v_pk_fma_f16 v71, v71, s60, v75 op_sel_hi:[1,0,1]
	v_and_b32_e32 v77, 0x7070707, v68
	v_and_b32_e32 v80, 0x7070707, v80
	v_perm_b32 v77, s2, v205, v77
	v_perm_b32 v80, s2, v205, v80
	v_lshlrev_b32_e32 v83, 4, v68
	v_and_or_b32 v77, v83, s4, v77
	v_and_or_b32 v68, v68, s4, v80
	v_perm_b32 v80, v68, v77, s5
	v_perm_b32 v83, v68, v77, s33
	v_perm_b32 v85, v68, v77, s0
	v_perm_b32 v68, v68, v77, s1
	v_pk_fma_f16 v77, v80, s36, v79 op_sel_hi:[1,0,1]
	v_pk_fma_f16 v79, v83, s36, v81 op_sel_hi:[1,0,1]
	v_lshrrev_b32_e32 v81, 4, v69
	v_pk_fma_f16 v68, v68, s36, v70 op_sel_hi:[1,0,1]
	v_and_b32_e32 v70, 0x7070707, v69
	v_and_b32_e32 v81, 0x7070707, v81
	v_pk_fma_f16 v80, v85, s36, v82 op_sel_hi:[1,0,1]
	v_perm_b32 v70, s2, v205, v70
	v_perm_b32 v81, s2, v205, v81
	v_lshlrev_b32_e32 v82, 4, v69
	v_and_or_b32 v70, v82, s4, v70
	v_and_or_b32 v69, v69, s4, v81
	v_perm_b32 v81, v69, v70, s5
	v_perm_b32 v82, v69, v70, s33
	v_perm_b32 v83, v69, v70, s0
	v_perm_b32 v69, v69, v70, s1
	v_pk_fma_f16 v70, v81, s36, v74 op_sel_hi:[1,0,1]
	v_pk_fma_f16 v74, v82, s36, v76 op_sel_hi:[1,0,1]
	v_pk_fma_f16 v76, v83, s36, v78 op_sel_hi:[1,0,1]
	v_readlane_b32 s59, v120, 28
	v_lshrrev_b32_e32 v78, 4, v64
	v_pk_fma_f16 v69, v69, s36, v71 op_sel_hi:[1,0,1]
	v_and_b32_e32 v75, 0x7070707, v64
	v_and_b32_e32 v78, 0x7070707, v78
	v_perm_b32 v75, s2, v205, v75
	v_perm_b32 v78, s2, v205, v78
	v_lshlrev_b32_e32 v81, 4, v64
	v_and_or_b32 v75, v81, s4, v75
	v_and_or_b32 v64, v64, s4, v78
	v_perm_b32 v78, v64, v75, s5
	v_perm_b32 v81, v64, v75, s33
	v_perm_b32 v82, v64, v75, s0
	v_perm_b32 v64, v64, v75, s1
	v_pk_fma_f16 v75, v78, s59, v77 op_sel_hi:[1,0,1]
	v_pk_fma_f16 v77, v81, s59, v79 op_sel_hi:[1,0,1]
	v_lshrrev_b32_e32 v79, 4, v65
	v_pk_fma_f16 v64, v64, s59, v68 op_sel_hi:[1,0,1]
	v_and_b32_e32 v68, 0x7070707, v65
	v_and_b32_e32 v79, 0x7070707, v79
	v_pk_fma_f16 v78, v82, s59, v80 op_sel_hi:[1,0,1]
	v_perm_b32 v68, s2, v205, v68
	v_perm_b32 v79, s2, v205, v79
	v_lshlrev_b32_e32 v80, 4, v65
	v_and_or_b32 v68, v80, s4, v68
	v_and_or_b32 v65, v65, s4, v79
	v_perm_b32 v79, v65, v68, s5
	v_perm_b32 v80, v65, v68, s33
	v_perm_b32 v81, v65, v68, s0
	v_perm_b32 v65, v65, v68, s1
	v_pk_fma_f16 v68, v79, s59, v70 op_sel_hi:[1,0,1]
	v_pk_fma_f16 v70, v80, s59, v74 op_sel_hi:[1,0,1]
	v_pk_fma_f16 v74, v81, s59, v76 op_sel_hi:[1,0,1]
	v_readlane_b32 s60, v120, 32
	v_lshrrev_b32_e32 v76, 4, v62
	v_pk_fma_f16 v65, v65, s59, v69 op_sel_hi:[1,0,1]
	v_and_b32_e32 v71, 0x7070707, v62
	v_and_b32_e32 v76, 0x7070707, v76
	v_perm_b32 v71, s2, v205, v71
	v_perm_b32 v76, s2, v205, v76
	v_lshlrev_b32_e32 v79, 4, v62
	v_and_or_b32 v71, v79, s4, v71
	v_and_or_b32 v62, v62, s4, v76
	v_perm_b32 v76, v62, v71, s5
	v_perm_b32 v79, v62, v71, s33
	v_perm_b32 v80, v62, v71, s0
	v_perm_b32 v62, v62, v71, s1
	v_pk_fma_f16 v71, v76, s60, v75 op_sel_hi:[1,0,1]
	v_pk_fma_f16 v75, v79, s60, v77 op_sel_hi:[1,0,1]
	v_lshrrev_b32_e32 v77, 4, v63
	v_pk_fma_f16 v62, v62, s60, v64 op_sel_hi:[1,0,1]
	v_and_b32_e32 v64, 0x7070707, v63
	v_and_b32_e32 v77, 0x7070707, v77
	v_pk_fma_f16 v76, v80, s60, v78 op_sel_hi:[1,0,1]
	v_perm_b32 v64, s2, v205, v64
	v_perm_b32 v77, s2, v205, v77
	v_lshlrev_b32_e32 v78, 4, v63
	v_and_or_b32 v64, v78, s4, v64
	v_and_or_b32 v63, v63, s4, v77
	v_perm_b32 v77, v63, v64, s5
	v_perm_b32 v78, v63, v64, s33
	v_perm_b32 v79, v63, v64, s0
	v_perm_b32 v63, v63, v64, s1
	v_pk_fma_f16 v64, v77, s60, v68 op_sel_hi:[1,0,1]
	v_pk_fma_f16 v68, v78, s60, v70 op_sel_hi:[1,0,1]
	v_pk_fma_f16 v70, v79, s60, v74 op_sel_hi:[1,0,1]
	v_readlane_b32 s36, v120, 36
	v_lshrrev_b32_e32 v74, 4, v66
	v_pk_fma_f16 v63, v63, s60, v65 op_sel_hi:[1,0,1]
	v_and_b32_e32 v69, 0x7070707, v66
	v_and_b32_e32 v74, 0x7070707, v74
	v_perm_b32 v69, s2, v205, v69
	v_perm_b32 v74, s2, v205, v74
	v_lshlrev_b32_e32 v77, 4, v66
	v_and_or_b32 v69, v77, s4, v69
	v_and_or_b32 v66, v66, s4, v74
	v_perm_b32 v74, v66, v69, s5
	v_perm_b32 v77, v66, v69, s33
	v_perm_b32 v78, v66, v69, s0
	v_perm_b32 v66, v66, v69, s1
	v_pk_fma_f16 v69, v74, s36, v71 op_sel_hi:[1,0,1]
	v_pk_fma_f16 v71, v77, s36, v75 op_sel_hi:[1,0,1]
	v_lshrrev_b32_e32 v75, 4, v67
	v_pk_fma_f16 v62, v66, s36, v62 op_sel_hi:[1,0,1]
	v_and_b32_e32 v66, 0x7070707, v67
	v_and_b32_e32 v75, 0x7070707, v75
	v_pk_fma_f16 v74, v78, s36, v76 op_sel_hi:[1,0,1]
	v_perm_b32 v66, s2, v205, v66
	v_perm_b32 v75, s2, v205, v75
	v_lshlrev_b32_e32 v76, 4, v67
	v_and_or_b32 v66, v76, s4, v66
	v_and_or_b32 v67, v67, s4, v75
	v_perm_b32 v76, v67, v66, s33
	v_perm_b32 v77, v67, v66, s0
	v_perm_b32 v75, v67, v66, s5
	v_perm_b32 v66, v67, v66, s1
	v_pk_fma_f16 v67, v76, s36, v68 op_sel_hi:[1,0,1]
	v_pk_fma_f16 v68, v77, s36, v70 op_sel_hi:[1,0,1]
	v_readlane_b32 s59, v120, 40
	v_lshrrev_b32_e32 v70, 4, v60
	v_pk_fma_f16 v64, v75, s36, v64 op_sel_hi:[1,0,1]
	v_pk_fma_f16 v63, v66, s36, v63 op_sel_hi:[1,0,1]
	v_and_b32_e32 v66, 0x7070707, v60
	v_and_b32_e32 v70, 0x7070707, v70
	v_perm_b32 v66, s2, v205, v66
	v_perm_b32 v70, s2, v205, v70
	v_lshlrev_b32_e32 v75, 4, v60
	v_and_or_b32 v66, v75, s4, v66
	v_and_or_b32 v60, v60, s4, v70
	v_perm_b32 v70, v60, v66, s5
	v_perm_b32 v75, v60, v66, s33
	v_perm_b32 v76, v60, v66, s0
	v_perm_b32 v60, v60, v66, s1
	v_pk_fma_f16 v66, v70, s59, v69 op_sel_hi:[1,0,1]
	v_pk_fma_f16 v69, v75, s59, v71 op_sel_hi:[1,0,1]
	v_lshrrev_b32_e32 v71, 4, v61
	v_pk_fma_f16 v60, v60, s59, v62 op_sel_hi:[1,0,1]
	v_and_b32_e32 v62, 0x7070707, v61
	v_and_b32_e32 v71, 0x7070707, v71
	v_pk_fma_f16 v70, v76, s59, v74 op_sel_hi:[1,0,1]
	v_perm_b32 v62, s2, v205, v62
	v_perm_b32 v71, s2, v205, v71
	v_lshlrev_b32_e32 v74, 4, v61
	v_and_or_b32 v62, v74, s4, v62
	v_and_or_b32 v61, v61, s4, v71
	v_perm_b32 v71, v61, v62, s5
	v_perm_b32 v74, v61, v62, s33
	v_perm_b32 v75, v61, v62, s0
	v_perm_b32 v61, v61, v62, s1
	v_pk_fma_f16 v62, v71, s59, v64 op_sel_hi:[1,0,1]
	v_pk_fma_f16 v64, v74, s59, v67 op_sel_hi:[1,0,1]
	v_pk_fma_f16 v67, v75, s59, v68 op_sel_hi:[1,0,1]
	v_readlane_b32 s60, v120, 44
	v_lshrrev_b32_e32 v68, 4, v58
	v_pk_fma_f16 v61, v61, s59, v63 op_sel_hi:[1,0,1]
	v_and_b32_e32 v65, 0x7070707, v58
	v_and_b32_e32 v68, 0x7070707, v68
	v_perm_b32 v65, s2, v205, v65
	v_perm_b32 v68, s2, v205, v68
	v_lshlrev_b32_e32 v71, 4, v58
	v_and_or_b32 v65, v71, s4, v65
	v_and_or_b32 v58, v58, s4, v68
	v_perm_b32 v68, v58, v65, s5
	v_perm_b32 v71, v58, v65, s33
	v_perm_b32 v74, v58, v65, s0
	v_perm_b32 v58, v58, v65, s1
	v_pk_fma_f16 v65, v68, s60, v66 op_sel_hi:[1,0,1]
	v_pk_fma_f16 v66, v71, s60, v69 op_sel_hi:[1,0,1]
	v_lshrrev_b32_e32 v69, 4, v59
	v_pk_fma_f16 v58, v58, s60, v60 op_sel_hi:[1,0,1]
	v_and_b32_e32 v60, 0x7070707, v59
	v_and_b32_e32 v69, 0x7070707, v69
	v_pk_fma_f16 v68, v74, s60, v70 op_sel_hi:[1,0,1]
	v_perm_b32 v60, s2, v205, v60
	v_perm_b32 v69, s2, v205, v69
	v_lshlrev_b32_e32 v70, 4, v59
	v_and_or_b32 v60, v70, s4, v60
	v_and_or_b32 v59, v59, s4, v69
	v_perm_b32 v69, v59, v60, s5
	v_perm_b32 v70, v59, v60, s33
	v_perm_b32 v71, v59, v60, s0
	v_perm_b32 v59, v59, v60, s1
	v_pk_fma_f16 v60, v69, s60, v62 op_sel_hi:[1,0,1]
	v_pk_fma_f16 v62, v70, s60, v64 op_sel_hi:[1,0,1]
	v_pk_fma_f16 v64, v71, s60, v67 op_sel_hi:[1,0,1]
	v_readlane_b32 s36, v120, 48
	v_lshrrev_b32_e32 v67, 4, v56
	v_pk_fma_f16 v59, v59, s60, v61 op_sel_hi:[1,0,1]
	v_and_b32_e32 v63, 0x7070707, v56
	v_and_b32_e32 v67, 0x7070707, v67
	v_perm_b32 v63, s2, v205, v63
	v_perm_b32 v67, s2, v205, v67
	v_lshlrev_b32_e32 v69, 4, v56
	v_and_or_b32 v63, v69, s4, v63
	v_and_or_b32 v56, v56, s4, v67
	v_perm_b32 v67, v56, v63, s5
	v_perm_b32 v69, v56, v63, s33
	v_perm_b32 v70, v56, v63, s0
	v_perm_b32 v56, v56, v63, s1
	v_pk_fma_f16 v63, v67, s36, v65 op_sel_hi:[1,0,1]
	v_lshrrev_b32_e32 v67, 4, v57
	v_pk_fma_f16 v56, v56, s36, v58 op_sel_hi:[1,0,1]
	v_and_b32_e32 v58, 0x7070707, v57
	v_and_b32_e32 v67, 0x7070707, v67
	v_pk_fma_f16 v65, v69, s36, v66 op_sel_hi:[1,0,1]
	v_pk_fma_f16 v66, v70, s36, v68 op_sel_hi:[1,0,1]
	v_perm_b32 v58, s2, v205, v58
	v_perm_b32 v67, s2, v205, v67
	v_lshlrev_b32_e32 v68, 4, v57
	v_and_or_b32 v58, v68, s4, v58
	v_and_or_b32 v57, v57, s4, v67
	v_perm_b32 v67, v57, v58, s5
	v_perm_b32 v68, v57, v58, s33
	v_perm_b32 v69, v57, v58, s0
	v_perm_b32 v57, v57, v58, s1
	v_pk_fma_f16 v58, v67, s36, v60 op_sel_hi:[1,0,1]
	v_pk_fma_f16 v60, v68, s36, v62 op_sel_hi:[1,0,1]
	v_pk_fma_f16 v62, v69, s36, v64 op_sel_hi:[1,0,1]
	v_readlane_b32 s59, v120, 52
	v_lshrrev_b32_e32 v64, 4, v54
	v_pk_fma_f16 v57, v57, s36, v59 op_sel_hi:[1,0,1]
	v_and_b32_e32 v61, 0x7070707, v54
	v_and_b32_e32 v64, 0x7070707, v64
	v_perm_b32 v61, s2, v205, v61
	v_perm_b32 v64, s2, v205, v64
	v_lshlrev_b32_e32 v67, 4, v54
	v_and_or_b32 v61, v67, s4, v61
	v_and_or_b32 v54, v54, s4, v64
	v_perm_b32 v64, v54, v61, s5
	v_perm_b32 v67, v54, v61, s33
	v_perm_b32 v68, v54, v61, s0
	v_perm_b32 v54, v54, v61, s1
	v_pk_fma_f16 v61, v64, s59, v63 op_sel_hi:[1,0,1]
	v_pk_fma_f16 v63, v67, s59, v65 op_sel_hi:[1,0,1]
	v_lshrrev_b32_e32 v65, 4, v55
	v_pk_fma_f16 v54, v54, s59, v56 op_sel_hi:[1,0,1]
	v_and_b32_e32 v56, 0x7070707, v55
	v_and_b32_e32 v65, 0x7070707, v65
	v_pk_fma_f16 v64, v68, s59, v66 op_sel_hi:[1,0,1]
	v_perm_b32 v56, s2, v205, v56
	v_perm_b32 v65, s2, v205, v65
	v_lshlrev_b32_e32 v66, 4, v55
	v_and_or_b32 v56, v66, s4, v56
	v_and_or_b32 v55, v55, s4, v65
	v_perm_b32 v65, v55, v56, s5
	v_perm_b32 v66, v55, v56, s33
	v_perm_b32 v67, v55, v56, s0
	v_perm_b32 v55, v55, v56, s1
	v_pk_fma_f16 v56, v65, s59, v58 op_sel_hi:[1,0,1]
	v_pk_fma_f16 v58, v66, s59, v60 op_sel_hi:[1,0,1]
	v_pk_fma_f16 v60, v67, s59, v62 op_sel_hi:[1,0,1]
	v_readlane_b32 s60, v120, 56
	v_lshrrev_b32_e32 v62, 4, v52
	v_pk_fma_f16 v55, v55, s59, v57 op_sel_hi:[1,0,1]
	v_and_b32_e32 v59, 0x7070707, v52
	v_and_b32_e32 v62, 0x7070707, v62
	v_perm_b32 v59, s2, v205, v59
	v_perm_b32 v62, s2, v205, v62
	v_lshlrev_b32_e32 v65, 4, v52
	v_and_or_b32 v59, v65, s4, v59
	v_and_or_b32 v52, v52, s4, v62
	v_perm_b32 v62, v52, v59, s5
	v_perm_b32 v65, v52, v59, s33
	v_perm_b32 v66, v52, v59, s0
	v_perm_b32 v52, v52, v59, s1
	v_pk_fma_f16 v59, v62, s60, v61 op_sel_hi:[1,0,1]
	v_pk_fma_f16 v61, v65, s60, v63 op_sel_hi:[1,0,1]
	v_lshrrev_b32_e32 v63, 4, v53
	v_pk_fma_f16 v52, v52, s60, v54 op_sel_hi:[1,0,1]
	v_and_b32_e32 v54, 0x7070707, v53
	v_and_b32_e32 v63, 0x7070707, v63
	v_pk_fma_f16 v62, v66, s60, v64 op_sel_hi:[1,0,1]
	v_perm_b32 v54, s2, v205, v54
	v_perm_b32 v63, s2, v205, v63
	v_lshlrev_b32_e32 v64, 4, v53
	v_and_or_b32 v54, v64, s4, v54
	v_and_or_b32 v53, v53, s4, v63
	v_perm_b32 v63, v53, v54, s5
	v_perm_b32 v64, v53, v54, s33
	v_perm_b32 v65, v53, v54, s0
	v_perm_b32 v53, v53, v54, s1
	v_pk_fma_f16 v54, v63, s60, v56 op_sel_hi:[1,0,1]
	v_pk_fma_f16 v56, v64, s60, v58 op_sel_hi:[1,0,1]
	v_pk_fma_f16 v58, v65, s60, v60 op_sel_hi:[1,0,1]
	v_readlane_b32 s36, v120, 60
	v_lshrrev_b32_e32 v60, 4, v36
	v_pk_fma_f16 v53, v53, s60, v55 op_sel_hi:[1,0,1]
	v_and_b32_e32 v57, 0x7070707, v36
	v_and_b32_e32 v60, 0x7070707, v60
	v_perm_b32 v57, s2, v205, v57
	v_perm_b32 v60, s2, v205, v60
	v_lshlrev_b32_e32 v63, 4, v36
	v_and_or_b32 v57, v63, s4, v57
	v_and_or_b32 v36, v36, s4, v60
	v_perm_b32 v60, v36, v57, s5
	v_perm_b32 v63, v36, v57, s33
	v_perm_b32 v64, v36, v57, s0
	v_perm_b32 v36, v36, v57, s1
	v_pk_fma_f16 v100, v36, s36, v52 op_sel_hi:[1,0,1]
	v_lshrrev_b32_e32 v52, 4, v37
	v_and_b32_e32 v36, 0x7070707, v37
	v_and_b32_e32 v52, 0x7070707, v52
	v_perm_b32 v36, s2, v205, v36
	v_perm_b32 v52, s2, v205, v52
	v_lshlrev_b32_e32 v57, 4, v37
	v_and_or_b32 v36, v57, s4, v36
	v_and_or_b32 v37, v37, s4, v52
	v_pk_fma_f16 v103, v60, s36, v59 op_sel_hi:[1,0,1]
	v_perm_b32 v52, v37, v36, s5
	v_perm_b32 v57, v37, v36, s33
	v_perm_b32 v59, v37, v36, s0
	v_perm_b32 v36, v37, v36, s1
	v_pk_fma_f16 v96, v36, s36, v53 op_sel_hi:[1,0,1]
	v_lshl_add_u64 v[36:37], v[6:7], 0, s[12:13]
	global_load_dwordx2 v[82:83], v[36:37], off
	v_lshl_add_u64 v[36:37], v[6:7], 0, s[14:15]
	global_load_dwordx2 v[80:81], v[36:37], off
	v_lshl_add_u64 v[40:41], v[4:5], 0, s[38:39]
	v_lshl_add_u64 v[36:37], v[6:7], 0, s[16:17]
	global_load_dwordx2 v[48:49], v[40:41], off
	global_load_dwordx2 v[78:79], v[36:37], off
	v_lshl_add_u64 v[40:41], v[4:5], 0, s[50:51]
	v_lshl_add_u64 v[36:37], v[6:7], 0, s[18:19]
	global_load_dwordx2 v[46:47], v[40:41], off
	global_load_dwordx2 v[76:77], v[36:37], off
	v_lshl_add_u64 v[40:41], v[4:5], 0, s[52:53]
	v_lshl_add_u64 v[36:37], v[6:7], 0, s[20:21]
	global_load_dwordx2 v[44:45], v[40:41], off
	global_load_dwordx2 v[74:75], v[36:37], off
	v_lshl_add_u64 v[40:41], v[4:5], 0, s[54:55]
	v_lshl_add_u64 v[36:37], v[6:7], 0, s[22:23]
	global_load_dwordx2 v[42:43], v[40:41], off
	global_load_dwordx2 v[70:71], v[36:37], off
	v_lshl_add_u64 v[40:41], v[4:5], 0, s[56:57]
	v_lshl_add_u64 v[36:37], v[6:7], 0, s[24:25]
	global_load_dwordx2 v[40:41], v[40:41], off
	v_pk_fma_f16 v101, v64, s36, v62 op_sel_hi:[1,0,1]
	global_load_dwordx2 v[68:69], v[36:37], off
	v_lshl_add_u64 v[36:37], v[6:7], 0, s[26:27]
	global_load_dwordx2 v[64:65], v[36:37], off
	v_lshl_add_u64 v[36:37], v[6:7], 0, s[28:29]
	v_pk_fma_f16 v102, v63, s36, v61 op_sel_hi:[1,0,1]
	global_load_dwordx2 v[62:63], v[36:37], off
	v_lshl_add_u64 v[36:37], v[6:7], 0, s[30:31]
	global_load_dwordx2 v[66:67], v[36:37], off
	v_lshl_add_u64 v[36:37], v[6:7], 0, s[34:35]
	global_load_dwordx2 v[60:61], v[36:37], off
	v_lshl_add_u64 v[36:37], v[6:7], 0, s[38:39]
	v_pk_fma_f16 v97, v59, s36, v58 op_sel_hi:[1,0,1]
	global_load_dwordx2 v[58:59], v[36:37], off
	v_lshl_add_u64 v[36:37], v[6:7], 0, s[50:51]
	v_pk_fma_f16 v98, v57, s36, v56 op_sel_hi:[1,0,1]
	global_load_dwordx2 v[56:57], v[36:37], off
	v_lshl_add_u64 v[36:37], v[6:7], 0, s[52:53]
	v_pk_fma_f16 v99, v52, s36, v54 op_sel_hi:[1,0,1]
	global_load_dwordx2 v[54:55], v[36:37], off
	v_lshl_add_u64 v[36:37], v[6:7], 0, s[54:55]
	global_load_dwordx2 v[52:53], v[36:37], off
	v_lshl_add_u64 v[36:37], v[6:7], 0, s[56:57]
	global_load_dwordx2 v[8:9], v[8:9], off
	s_cmpk_eq_i32 s58, 0x90
	global_load_dwordx2 v[10:11], v[10:11], off
	s_nop 0
	global_load_dwordx2 v[12:13], v[12:13], off
	s_nop 0
	global_load_dwordx2 v[14:15], v[14:15], off
	s_nop 0
	global_load_dwordx2 v[16:17], v[16:17], off
	s_nop 0
	global_load_dwordx2 v[18:19], v[18:19], off
	s_nop 0
	global_load_dwordx2 v[20:21], v[20:21], off
	s_nop 0
	global_load_dwordx2 v[22:23], v[22:23], off
	s_nop 0
	global_load_dwordx2 v[36:37], v[36:37], off
	s_cbranch_scc0 .LBB0_763
	v_lshlrev_b64 v[0:1], 2, v[2:3]
	v_lshl_add_u64 v[2:3], v[28:29], 0, v[0:1]
	v_mov_b32_e32 v104, v208
	v_mov_b32_e32 v105, v209
	v_mov_b32_e32 v106, v210
	v_mov_b32_e32 v107, v211
	v_mov_b32_e32 v108, v212
	v_mov_b32_e32 v109, v213
	v_mov_b32_e32 v110, v214
	v_mov_b32_e32 v111, v215
	v_mov_b32_e32 v86, v216
	v_mov_b32_e32 v87, v217
	v_mov_b32_e32 v88, v218
	v_mov_b32_e32 v89, v219
	v_mov_b32_e32 v112, v220
	v_mov_b32_e32 v113, v221
	v_mov_b32_e32 v114, v222
	v_mov_b32_e32 v115, v223
	v_lshl_add_u64 v[72:73], v[32:33], 0, v[0:1]
	v_cvt_f32_f16_sdwa v1, v103 dst_sel:DWORD dst_unused:UNUSED_PAD src0_sel:WORD_1
	v_cvt_f32_f16_e32 v0, v103
	v_cvt_f32_f16_sdwa v91, v102 dst_sel:DWORD dst_unused:UNUSED_PAD src0_sel:WORD_1
	v_cvt_f32_f16_e32 v90, v102
	v_cvt_f32_f16_sdwa v103, v101 dst_sel:DWORD dst_unused:UNUSED_PAD src0_sel:WORD_1
	v_cvt_f32_f16_e32 v102, v101
	v_cvt_f32_f16_sdwa v101, v100 dst_sel:DWORD dst_unused:UNUSED_PAD src0_sel:WORD_1
	v_cvt_f32_f16_e32 v100, v100
	s_mov_b32 s18, 0x800000
	v_readlane_b32 s12, v255, 5
	v_readlane_b32 s13, v255, 6
	v_pk_add_f32 v[86:87], v[86:87], v[102:103]
	v_pk_add_f32 v[84:85], v[112:113], v[0:1]
	v_mov_b32_e32 v102, v85
	v_mov_b32_e32 v103, v87
	v_pk_add_f32 v[90:91], v[114:115], v[90:91]
	v_pk_add_f32 v[88:89], v[88:89], v[100:101]
	v_mov_b32_e32 v100, v84
	v_mov_b32_e32 v101, v86
	v_pk_mul_f32 v[102:103], v[102:103], v[102:103]
	v_mov_b32_e32 v112, v91
	v_pk_fma_f32 v[100:101], v[100:101], v[100:101], v[102:103]
	v_mov_b32_e32 v102, v90
	v_mov_b32_e32 v103, v88
	v_pk_fma_f32 v[100:101], v[102:103], v[102:103], v[100:101]
	v_cvt_f32_f16_sdwa v103, v99 dst_sel:DWORD dst_unused:UNUSED_PAD src0_sel:WORD_1
	v_cvt_f32_f16_e32 v102, v99
	v_cvt_f32_f16_sdwa v99, v98 dst_sel:DWORD dst_unused:UNUSED_PAD src0_sel:WORD_1
	v_cvt_f32_f16_e32 v98, v98
	v_mov_b32_e32 v113, v89
	v_pk_add_f32 v[102:103], v[108:109], v[102:103]
	v_cvt_f32_f16_sdwa v109, v97 dst_sel:DWORD dst_unused:UNUSED_PAD src0_sel:WORD_1
	v_cvt_f32_f16_e32 v108, v97
	v_cvt_f32_f16_sdwa v97, v96 dst_sel:DWORD dst_unused:UNUSED_PAD src0_sel:WORD_1
	v_cvt_f32_f16_e32 v96, v96
	v_pk_add_f32 v[98:99], v[110:111], v[98:99]
	v_pk_add_f32 v[104:105], v[104:105], v[108:109]
	v_mov_b32_e32 v108, v103
	v_mov_b32_e32 v109, v105
	v_pk_add_f32 v[96:97], v[106:107], v[96:97]
	v_mov_b32_e32 v106, v102
	v_mov_b32_e32 v107, v104
	v_pk_mul_f32 v[108:109], v[108:109], v[108:109]
	v_pk_fma_f32 v[100:101], v[112:113], v[112:113], v[100:101]
	v_pk_fma_f32 v[106:107], v[106:107], v[106:107], v[108:109]
	v_mov_b32_e32 v108, v98
	v_mov_b32_e32 v109, v96
	v_mov_b32_e32 v110, v99
	v_mov_b32_e32 v111, v97
	v_pk_fma_f32 v[106:107], v[108:109], v[108:109], v[106:107]
	v_add_f32_e32 v95, v100, v101
	v_pk_fma_f32 v[106:107], v[110:111], v[110:111], v[106:107]
	v_lshl_add_u64 v[34:35], v[34:35], 0, s[12:13]
	v_add_f32_e32 v95, v95, v106
	v_add_f32_e32 v95, v95, v107
	ds_bpermute_b32 v100, v184, v95
	s_waitcnt lgkmcnt(0)
	v_add_f32_e32 v95, v95, v100
	ds_bpermute_b32 v100, v185, v95
	s_waitcnt lgkmcnt(0)
	v_add_f32_e32 v95, v95, v100
	ds_bpermute_b32 v100, v186, v95
	s_waitcnt lgkmcnt(0)
	v_add_f32_e32 v95, v95, v100
	ds_bpermute_b32 v100, v187, v95
	s_waitcnt lgkmcnt(0)
	v_add_f32_e32 v95, v95, v100
	ds_bpermute_b32 v100, v188, v95
	s_waitcnt lgkmcnt(0)
	v_add_f32_e32 v95, v95, v100
	ds_bpermute_b32 v100, v189, v95
	s_waitcnt lgkmcnt(0)
	v_add_f32_e32 v95, v95, v100
	v_fmamk_f32 v95, v95, 0x3a800000, v191
	v_cmp_gt_f32_e32 vcc, s18, v95
	v_mul_f32_e32 v100, 0x4b800000, v95
	s_nop 0
	v_cndmask_b32_e32 v95, v95, v100, vcc
	v_rsq_f32_e32 v95, v95
	s_nop 0
	v_mul_f32_e32 v100, 0x45800000, v95
	v_cndmask_b32_e32 v100, v95, v100, vcc
	v_pk_mul_f32 v[84:85], v[84:85], v[100:101] op_sel_hi:[1,0]
	v_pk_mul_f32 v[0:1], v[124:125], v[84:85]
	v_pk_mul_f32 v[84:85], v[90:91], v[100:101] op_sel_hi:[1,0]
	s_nop 0
	v_pk_mul_f32 v[2:3], v[126:127], v[84:85]
	global_store_dwordx4 v[72:73], v[0:3], off
	s_nop 1
	v_pk_mul_f32 v[84:85], v[86:87], v[100:101] op_sel_hi:[1,0]
	v_pk_mul_f32 v[0:1], v[128:129], v[84:85]
	v_pk_mul_f32 v[84:85], v[88:89], v[100:101] op_sel_hi:[1,0]
	s_nop 0
	v_pk_mul_f32 v[2:3], v[130:131], v[84:85]
	global_store_dwordx4 v[72:73], v[0:3], off offset:16
	s_nop 1
	v_pk_mul_f32 v[84:85], v[102:103], v[100:101] op_sel_hi:[1,0]
	v_pk_mul_f32 v[0:1], v[84:85], v[132:133]
	v_pk_mul_f32 v[84:85], v[98:99], v[100:101] op_sel_hi:[1,0]
	s_nop 0
	v_pk_mul_f32 v[2:3], v[84:85], v[134:135]
	global_store_dwordx4 v[72:73], v[0:3], off offset:32
	s_nop 1
	v_pk_mul_f32 v[84:85], v[104:105], v[100:101] op_sel_hi:[1,0]
	v_pk_mul_f32 v[0:1], v[84:85], v[136:137]
	v_pk_mul_f32 v[84:85], v[96:97], v[100:101] op_sel_hi:[1,0]
	s_nop 0
	v_pk_mul_f32 v[2:3], v[84:85], v[138:139]
	global_store_dwordx4 v[72:73], v[0:3], off offset:48
	s_nop 1
	v_mov_b32_e32 v0, v94
	s_andn2_b64 exec, exec, s[10:11]
	s_cbranch_execnz .LBB0_762

.LBB0_770:
	s_cmpk_eq_i32 s56, 0x80
	s_cselect_b64 s[10:11], -1, 0
	ds_bpermute_b32 v6, v97, v96
	s_and_b64 vcc, s[10:11], s[48:49]
	v_cndmask_b32_e32 v94, v0, v98, vcc
	v_ashrrev_i32_e32 v95, 31, v94
	s_and_b32 s10, s56, 0x70
	v_lshlrev_b64 v[94:95], 9, v[94:95]
	v_lshl_add_u64 v[94:95], s[94:95], 0, v[94:95]
	s_lshl_b32 s36, s10, 2
	s_waitcnt lgkmcnt(0)
	v_ashrrev_i32_e32 v7, 31, v6
	v_lshl_add_u64 v[94:95], v[94:95], 0, s[36:37]
	v_lshl_add_u64 v[6:7], v[6:7], 3, s[88:89]
	v_lshl_add_u64 v[94:95], v[94:95], 0, v[144:145]
	global_load_dwordx2 v[6:7], v[6:7], off
	s_nop 0
	global_load_dword v8, v[4:5], off
	global_load_dword v96, v[94:95], off
	s_waitcnt vmcnt(33)
	v_dot8_i32_i4 v9, v20, v1, 0
	v_dot8_i32_i4 v94, v20, v10, 0
	v_dot8_i32_i4 v9, v21, v11, v9
	v_dot8_i32_i4 v94, v21, v12, v94
	v_dot8_i32_i4 v20, v22, v1, 0
	v_dot8_i32_i4 v21, v22, v10, 0
	v_dot8_i32_i4 v20, v23, v11, v20
	v_dot8_i32_i4 v21, v23, v12, v21
	v_lshl_add_u32 v9, v9, 4, v94
	v_cvt_f32_i32_e32 v9, v9
	s_add_i32 s56, s56, 16
	v_lshl_add_u32 v20, v20, 4, v21
	v_cvt_f32_i32_e32 v94, v20
	s_waitcnt vmcnt(32)
	v_dot8_i32_i4 v20, v24, v1, 0
	v_dot8_i32_i4 v21, v24, v10, 0
	v_dot8_i32_i4 v20, v25, v11, v20
	v_dot8_i32_i4 v21, v25, v12, v21
	v_lshl_add_u64 v[4:5], v[4:5], 0, 64
	s_waitcnt vmcnt(2)
	v_mul_f32_e32 v7, v13, v7
	v_lshl_add_u32 v20, v20, 4, v21
	v_cvt_f32_i32_e32 v95, v20
	v_dot8_i32_i4 v20, v26, v1, 0
	v_dot8_i32_i4 v21, v26, v10, 0
	v_dot8_i32_i4 v20, v27, v11, v20
	v_dot8_i32_i4 v21, v27, v12, v21
	s_waitcnt vmcnt(0)
	v_readlane_b32 s10, v96, 0
	s_ashr_i32 s11, s10, 31
	v_readlane_b32 s12, v96, 1
	v_lshl_add_u32 v20, v20, 4, v21
	v_cvt_f32_i32_e32 v106, v20
	v_dot8_i32_i4 v20, v28, v1, 0
	v_dot8_i32_i4 v21, v28, v10, 0
	v_dot8_i32_i4 v20, v29, v11, v20
	v_dot8_i32_i4 v21, v29, v12, v21
	s_lshl_b64 s[10:11], s[10:11], 9
	s_ashr_i32 s13, s12, 31
	v_readlane_b32 s14, v96, 2
	v_lshl_add_u32 v20, v20, 4, v21
	v_cvt_f32_i32_e32 v107, v20
	v_dot8_i32_i4 v20, v30, v1, 0
	v_dot8_i32_i4 v21, v30, v10, 0
	v_dot8_i32_i4 v20, v31, v11, v20
	v_dot8_i32_i4 v21, v31, v12, v21
	s_lshl_b64 s[12:13], s[12:13], 9
	s_ashr_i32 s15, s14, 31
	v_readlane_b32 s16, v96, 3
	v_lshl_add_u32 v20, v20, 4, v21
	v_cvt_f32_i32_e32 v108, v20
	v_dot8_i32_i4 v20, v32, v1, 0
	v_dot8_i32_i4 v21, v32, v10, 0
	v_dot8_i32_i4 v20, v33, v11, v20
	v_dot8_i32_i4 v21, v33, v12, v21
	v_lshl_add_u64 v[22:23], v[16:17], 0, s[12:13]
	s_lshl_b64 s[14:15], s[14:15], 9
	s_ashr_i32 s17, s16, 31
	v_lshl_add_u32 v20, v20, 4, v21
	v_cvt_f32_i32_e32 v109, v20
	v_dot8_i32_i4 v20, v34, v1, 0
	v_dot8_i32_i4 v21, v34, v10, 0
	v_dot8_i32_i4 v20, v35, v11, v20
	v_dot8_i32_i4 v21, v35, v12, v21
	v_readlane_b32 s18, v96, 4
	global_load_dwordx2 v[22:23], v[22:23], off
	v_lshl_add_u64 v[24:25], v[16:17], 0, s[14:15]
	v_lshl_add_u32 v20, v20, 4, v21
	v_cvt_f32_i32_e32 v110, v20
	v_dot8_i32_i4 v20, v36, v1, 0
	v_dot8_i32_i4 v21, v36, v10, 0
	v_dot8_i32_i4 v20, v37, v11, v20
	v_dot8_i32_i4 v21, v37, v12, v21
	s_lshl_b64 s[16:17], s[16:17], 9
	s_ashr_i32 s19, s18, 31
	v_readlane_b32 s20, v96, 5
	v_lshl_add_u32 v20, v20, 4, v21
	v_cvt_f32_i32_e32 v111, v20
	v_dot8_i32_i4 v20, v38, v1, 0
	v_dot8_i32_i4 v21, v38, v10, 0
	v_dot8_i32_i4 v20, v39, v11, v20
	v_dot8_i32_i4 v21, v39, v12, v21
	v_permlane32_swap_b32 v9, v111
	s_nop 1
	v_lshl_add_u32 v20, v20, 4, v21
	v_cvt_f32_i32_e32 v112, v20
	v_dot8_i32_i4 v20, v40, v1, 0
	v_dot8_i32_i4 v21, v40, v10, 0
	v_dot8_i32_i4 v20, v41, v11, v20
	v_dot8_i32_i4 v21, v41, v12, v21
	s_waitcnt lgkmcnt(0)
	v_add_f32_e32 v9, v9, v111
	v_permlane32_swap_b32 v94, v112
	v_lshl_add_u32 v20, v20, 4, v21
	v_cvt_f32_i32_e32 v113, v20
	v_dot8_i32_i4 v20, v60, v1, 0
	v_dot8_i32_i4 v21, v60, v10, 0
	v_dot8_i32_i4 v20, v61, v11, v20
	v_dot8_i32_i4 v21, v61, v12, v21
	s_waitcnt lgkmcnt(0)
	v_add_f32_e32 v94, v94, v112
	v_permlane32_swap_b32 v95, v113
	v_lshl_add_u32 v20, v20, 4, v21
	v_cvt_f32_i32_e32 v114, v20
	v_dot8_i32_i4 v20, v58, v1, 0
	v_dot8_i32_i4 v21, v58, v10, 0
	v_dot8_i32_i4 v20, v59, v11, v20
	v_dot8_i32_i4 v21, v59, v12, v21
	s_waitcnt lgkmcnt(0)
	v_add_f32_e32 v95, v95, v113
	v_permlane32_swap_b32 v106, v114
	v_lshl_add_u32 v20, v20, 4, v21
	v_cvt_f32_i32_e32 v115, v20
	v_dot8_i32_i4 v20, v56, v1, 0
	v_dot8_i32_i4 v21, v56, v10, 0
	v_dot8_i32_i4 v20, v57, v11, v20
	v_dot8_i32_i4 v21, v57, v12, v21
	s_waitcnt lgkmcnt(0)
	v_add_f32_e32 v106, v106, v114
	v_permlane32_swap_b32 v107, v115
	v_lshl_add_u32 v20, v20, 4, v21
	v_cvt_f32_i32_e32 v116, v20
	v_dot8_i32_i4 v20, v54, v1, 0
	v_dot8_i32_i4 v21, v54, v10, 0
	v_dot8_i32_i4 v20, v55, v11, v20
	v_dot8_i32_i4 v21, v55, v12, v21
	s_waitcnt lgkmcnt(0)
	v_add_f32_e32 v107, v107, v115
	v_permlane32_swap_b32 v108, v116
	v_lshl_add_u32 v20, v20, 4, v21
	v_cvt_f32_i32_e32 v117, v20
	v_dot8_i32_i4 v20, v52, v1, 0
	v_dot8_i32_i4 v21, v52, v10, 0
	v_dot8_i32_i4 v20, v53, v11, v20
	v_dot8_i32_i4 v21, v53, v12, v21
	s_waitcnt lgkmcnt(0)
	v_add_f32_e32 v108, v108, v116
	v_permlane32_swap_b32 v109, v117
	v_lshl_add_u32 v20, v20, 4, v21
	v_cvt_f32_i32_e32 v118, v20
	v_lshl_add_u64 v[20:21], v[16:17], 0, s[10:11]
	s_waitcnt lgkmcnt(0)
	v_add_f32_e32 v109, v109, v117
	v_permlane32_swap_b32 v110, v118
	global_load_dwordx2 v[20:21], v[20:21], off
	v_lshl_add_u64 v[26:27], v[16:17], 0, s[16:17]
	global_load_dwordx2 v[24:25], v[24:25], off
	s_waitcnt lgkmcnt(0)
	v_add_f32_e32 v110, v110, v118
	v_permlane16_swap_b32 v9, v107
	s_lshl_b64 s[18:19], s[18:19], 9
	s_ashr_i32 s21, s20, 31
	v_readlane_b32 s22, v96, 6
	global_load_dwordx2 v[26:27], v[26:27], off
	s_waitcnt lgkmcnt(0)
	v_add_f32_e32 v9, v9, v107
	v_permlane16_swap_b32 v94, v108
	v_lshl_add_u64 v[28:29], v[16:17], 0, s[18:19]
	s_lshl_b64 s[20:21], s[20:21], 9
	s_ashr_i32 s23, s22, 31
	s_waitcnt lgkmcnt(0)
	v_add_f32_e32 v94, v94, v108
	v_permlane16_swap_b32 v95, v109
	v_readlane_b32 s24, v96, 7
	global_load_dwordx2 v[28:29], v[28:29], off
	v_lshl_add_u64 v[30:31], v[16:17], 0, s[20:21]
	s_waitcnt lgkmcnt(0)
	v_add_f32_e32 v95, v95, v109
	v_permlane16_swap_b32 v106, v110
	s_lshl_b64 s[22:23], s[22:23], 9
	s_ashr_i32 s25, s24, 31
	v_readlane_b32 s26, v96, 8
	s_waitcnt lgkmcnt(0)
	v_add_f32_e32 v106, v106, v110
	v_cndmask_b32_e64 v107, v9, v95, s[44:45]
	v_cndmask_b32_e64 v9, v95, v9, s[44:45]
	ds_bpermute_b32 v95, v186, v107
	global_load_dwordx2 v[30:31], v[30:31], off
	v_lshl_add_u64 v[32:33], v[16:17], 0, s[22:23]
	s_lshl_b64 s[24:25], s[24:25], 9
	s_ashr_i32 s27, s26, 31
	s_waitcnt lgkmcnt(0)
	v_add_f32_e32 v9, v9, v95
	v_cndmask_b32_e64 v95, v94, v106, s[44:45]
	ds_bpermute_b32 v95, v186, v95
	v_cndmask_b32_e64 v94, v106, v94, s[44:45]
	v_readlane_b32 s28, v96, 9
	global_load_dwordx2 v[32:33], v[32:33], off
	v_lshl_add_u64 v[34:35], v[16:17], 0, s[24:25]
	s_waitcnt lgkmcnt(0)
	v_add_f32_e32 v94, v94, v95
	v_cndmask_b32_e64 v95, v9, v94, s[46:47]
	v_cndmask_b32_e64 v9, v94, v9, s[46:47]
	ds_bpermute_b32 v94, v187, v95
	s_lshl_b64 s[26:27], s[26:27], 9
	s_ashr_i32 s29, s28, 31
	v_readlane_b32 s30, v96, 10
	global_load_dwordx2 v[34:35], v[34:35], off
	s_waitcnt lgkmcnt(0)
	v_add_f32_e32 v9, v9, v94
	ds_bpermute_b32 v94, v188, v9
	v_lshl_add_u64 v[36:37], v[16:17], 0, s[26:27]
	s_lshl_b64 s[28:29], s[28:29], 9
	s_ashr_i32 s31, s30, 31
	v_readlane_b32 s34, v96, 11
	s_waitcnt lgkmcnt(0)
	v_add_f32_e32 v9, v9, v94
	ds_bpermute_b32 v94, v189, v9
	global_load_dwordx2 v[36:37], v[36:37], off
	v_lshl_add_u64 v[38:39], v[16:17], 0, s[28:29]
	s_lshl_b64 s[30:31], s[30:31], 9
	s_ashr_i32 s35, s34, 31
	s_waitcnt lgkmcnt(0)
	v_add_f32_e32 v9, v9, v94
	v_add_f32_e32 v9, v14, v9
	v_mul_f32_e32 v7, v7, v9
	v_mul_f32_e32 v9, 0x3d372713, v7
	v_mul_f32_e32 v9, v7, v9
	v_fma_f32 v9, v7, v9, v7
	v_mul_f32_e32 v9, 0x3fcc422a, v9
	v_mul_f32_e32 v9, 0xbfb8aa3b, v9
	v_exp_f32_e32 v9, v9
	v_lshlrev_b32_e32 v94, 4, v92
	v_readlane_b32 s38, v96, 12
	global_load_dwordx2 v[38:39], v[38:39], off
	v_add_f32_e32 v9, 1.0, v9
	v_rcp_f32_e32 v9, v9
	v_lshl_add_u64 v[40:41], v[16:17], 0, s[30:31]
	s_lshl_b64 s[34:35], s[34:35], 9
	s_ashr_i32 s39, s38, 31
	v_pk_mul_f32 v[6:7], v[6:7], v[8:9]
	v_lshrrev_b32_e32 v9, 4, v92
	v_pk_mul_f32 v[6:7], v[6:7], v[6:7] op_sel:[0,1] op_sel_hi:[1,0]
	v_cvt_f16_f32_e32 v120, v6
	v_and_b32_e32 v8, 0x7070707, v92
	v_readlane_b32 s36, v120, 0
	v_and_b32_e32 v9, 0x7070707, v9
	v_perm_b32 v8, s2, v205, v8
	v_perm_b32 v9, s2, v205, v9
	v_and_or_b32 v8, v94, s4, v8
	v_and_or_b32 v9, v92, s4, v9
	v_perm_b32 v92, v9, v8, s5
	v_perm_b32 v94, v9, v8, s33
	v_perm_b32 v95, v9, v8, s0
	v_perm_b32 v8, v9, v8, s1
	v_pk_fma_f16 v8, v8, s36, v102 op_sel_hi:[1,0,1]
	v_lshrrev_b32_e32 v102, 4, v93
	v_pk_fma_f16 v9, v92, s36, v105 op_sel_hi:[1,0,1]
	v_pk_fma_f16 v92, v94, s36, v104 op_sel_hi:[1,0,1]
	v_pk_fma_f16 v94, v95, s36, v103 op_sel_hi:[1,0,1]
	v_and_b32_e32 v95, 0x7070707, v93
	v_and_b32_e32 v102, 0x7070707, v102
	v_perm_b32 v95, s2, v205, v95
	v_perm_b32 v102, s2, v205, v102
	v_lshlrev_b32_e32 v103, 4, v93
	v_and_or_b32 v95, v103, s4, v95
	v_and_or_b32 v93, v93, s4, v102
	v_perm_b32 v102, v93, v95, s5
	v_perm_b32 v103, v93, v95, s33
	v_perm_b32 v104, v93, v95, s0
	v_perm_b32 v93, v93, v95, s1
	v_pk_fma_f16 v95, v102, s36, v101 op_sel_hi:[1,0,1]
	v_readlane_b32 s59, v120, 4
	v_lshrrev_b32_e32 v101, 4, v90
	v_pk_fma_f16 v100, v103, s36, v100 op_sel_hi:[1,0,1]
	v_pk_fma_f16 v99, v104, s36, v99 op_sel_hi:[1,0,1]
	v_pk_fma_f16 v7, v93, s36, v15 op_sel_hi:[1,0,1]
	v_and_b32_e32 v93, 0x7070707, v90
	v_and_b32_e32 v101, 0x7070707, v101
	v_perm_b32 v93, s2, v205, v93
	v_perm_b32 v101, s2, v205, v101
	v_lshlrev_b32_e32 v102, 4, v90
	v_and_or_b32 v93, v102, s4, v93
	v_and_or_b32 v90, v90, s4, v101
	v_perm_b32 v103, v90, v93, s0
	v_perm_b32 v101, v90, v93, s5
	v_perm_b32 v102, v90, v93, s33
	v_perm_b32 v90, v90, v93, s1
	v_pk_fma_f16 v93, v103, s59, v94 op_sel_hi:[1,0,1]
	v_lshrrev_b32_e32 v94, 4, v91
	v_pk_fma_f16 v8, v90, s59, v8 op_sel_hi:[1,0,1]
	v_and_b32_e32 v90, 0x7070707, v91
	v_and_b32_e32 v94, 0x7070707, v94
	v_pk_fma_f16 v9, v101, s59, v9 op_sel_hi:[1,0,1]
	v_perm_b32 v90, s2, v205, v90
	v_perm_b32 v94, s2, v205, v94
	v_lshlrev_b32_e32 v101, 4, v91
	v_and_or_b32 v90, v101, s4, v90
	v_and_or_b32 v91, v91, s4, v94
	v_pk_fma_f16 v92, v102, s59, v92 op_sel_hi:[1,0,1]
	v_perm_b32 v94, v91, v90, s5
	v_perm_b32 v102, v91, v90, s0
	v_perm_b32 v101, v91, v90, s33
	v_perm_b32 v90, v91, v90, s1
	v_pk_fma_f16 v91, v94, s59, v95 op_sel_hi:[1,0,1]
	v_pk_fma_f16 v95, v102, s59, v99 op_sel_hi:[1,0,1]
	v_readlane_b32 s60, v120, 8
	v_lshrrev_b32_e32 v99, 4, v88
	v_pk_fma_f16 v94, v101, s59, v100 op_sel_hi:[1,0,1]
	v_pk_fma_f16 v7, v90, s59, v7 op_sel_hi:[1,0,1]
	v_and_b32_e32 v90, 0x7070707, v88
	v_and_b32_e32 v99, 0x7070707, v99
	v_perm_b32 v90, s2, v205, v90
	v_perm_b32 v99, s2, v205, v99
	v_lshlrev_b32_e32 v100, 4, v88
	v_and_or_b32 v90, v100, s4, v90
	v_and_or_b32 v88, v88, s4, v99
	v_perm_b32 v100, v88, v90, s33
	v_perm_b32 v101, v88, v90, s0
	v_perm_b32 v99, v88, v90, s5
	v_perm_b32 v88, v88, v90, s1
	v_pk_fma_f16 v90, v100, s60, v92 op_sel_hi:[1,0,1]
	v_pk_fma_f16 v92, v101, s60, v93 op_sel_hi:[1,0,1]
	v_lshrrev_b32_e32 v93, 4, v89
	v_pk_fma_f16 v8, v88, s60, v8 op_sel_hi:[1,0,1]
	v_and_b32_e32 v88, 0x7070707, v89
	v_and_b32_e32 v93, 0x7070707, v93
	v_pk_fma_f16 v9, v99, s60, v9 op_sel_hi:[1,0,1]
	v_perm_b32 v88, s2, v205, v88
	v_perm_b32 v93, s2, v205, v93
	v_lshlrev_b32_e32 v99, 4, v89
	v_and_or_b32 v88, v99, s4, v88
	v_and_or_b32 v89, v89, s4, v93
	v_perm_b32 v93, v89, v88, s5
	v_perm_b32 v99, v89, v88, s33
	v_perm_b32 v100, v89, v88, s0
	v_perm_b32 v88, v89, v88, s1
	v_pk_fma_f16 v89, v93, s60, v91 op_sel_hi:[1,0,1]
	v_pk_fma_f16 v91, v99, s60, v94 op_sel_hi:[1,0,1]
	v_readlane_b32 s36, v120, 12
	v_lshrrev_b32_e32 v94, 4, v86
	v_pk_fma_f16 v93, v100, s60, v95 op_sel_hi:[1,0,1]
	v_pk_fma_f16 v7, v88, s60, v7 op_sel_hi:[1,0,1]
	v_and_b32_e32 v88, 0x7070707, v86
	v_and_b32_e32 v94, 0x7070707, v94
	v_perm_b32 v88, s2, v205, v88
	v_perm_b32 v94, s2, v205, v94
	v_lshlrev_b32_e32 v95, 4, v86
	v_and_or_b32 v88, v95, s4, v88
	v_and_or_b32 v86, v86, s4, v94
	v_perm_b32 v95, v86, v88, s33
	v_perm_b32 v99, v86, v88, s0
	v_perm_b32 v94, v86, v88, s5
	v_perm_b32 v86, v86, v88, s1
	v_pk_fma_f16 v88, v95, s36, v90 op_sel_hi:[1,0,1]
	v_pk_fma_f16 v90, v99, s36, v92 op_sel_hi:[1,0,1]
	v_lshrrev_b32_e32 v92, 4, v87
	v_pk_fma_f16 v8, v86, s36, v8 op_sel_hi:[1,0,1]
	v_and_b32_e32 v86, 0x7070707, v87
	v_and_b32_e32 v92, 0x7070707, v92
	v_pk_fma_f16 v9, v94, s36, v9 op_sel_hi:[1,0,1]
	v_perm_b32 v86, s2, v205, v86
	v_perm_b32 v92, s2, v205, v92
	v_lshlrev_b32_e32 v94, 4, v87
	v_and_or_b32 v86, v94, s4, v86
	v_and_or_b32 v87, v87, s4, v92
	v_perm_b32 v92, v87, v86, s5
	v_perm_b32 v94, v87, v86, s33
	v_perm_b32 v95, v87, v86, s0
	v_perm_b32 v86, v87, v86, s1
	v_pk_fma_f16 v87, v92, s36, v89 op_sel_hi:[1,0,1]
	v_readlane_b32 s59, v120, 16
	v_lshrrev_b32_e32 v92, 4, v84
	v_pk_fma_f16 v89, v94, s36, v91 op_sel_hi:[1,0,1]
	v_pk_fma_f16 v91, v95, s36, v93 op_sel_hi:[1,0,1]
	v_pk_fma_f16 v7, v86, s36, v7 op_sel_hi:[1,0,1]
	v_and_b32_e32 v86, 0x7070707, v84
	v_and_b32_e32 v92, 0x7070707, v92
	v_perm_b32 v86, s2, v205, v86
	v_perm_b32 v92, s2, v205, v92
	v_lshlrev_b32_e32 v93, 4, v84
	v_and_or_b32 v86, v93, s4, v86
	v_and_or_b32 v84, v84, s4, v92
	v_perm_b32 v93, v84, v86, s33
	v_perm_b32 v94, v84, v86, s0
	v_perm_b32 v92, v84, v86, s5
	v_perm_b32 v84, v84, v86, s1
	v_pk_fma_f16 v86, v93, s59, v88 op_sel_hi:[1,0,1]
	v_pk_fma_f16 v88, v94, s59, v90 op_sel_hi:[1,0,1]
	v_lshrrev_b32_e32 v90, 4, v85
	v_pk_fma_f16 v8, v84, s59, v8 op_sel_hi:[1,0,1]
	v_and_b32_e32 v84, 0x7070707, v85
	v_and_b32_e32 v90, 0x7070707, v90
	v_pk_fma_f16 v9, v92, s59, v9 op_sel_hi:[1,0,1]
	v_perm_b32 v84, s2, v205, v84
	v_perm_b32 v90, s2, v205, v90
	v_lshlrev_b32_e32 v92, 4, v85
	v_and_or_b32 v84, v92, s4, v84
	v_and_or_b32 v85, v85, s4, v90
	v_perm_b32 v90, v85, v84, s5
	v_perm_b32 v92, v85, v84, s33
	v_perm_b32 v93, v85, v84, s0
	v_perm_b32 v84, v85, v84, s1
	v_pk_fma_f16 v85, v90, s59, v87 op_sel_hi:[1,0,1]
	v_readlane_b32 s60, v120, 20
	v_lshrrev_b32_e32 v90, 4, v82
	v_pk_fma_f16 v87, v92, s59, v89 op_sel_hi:[1,0,1]
	v_pk_fma_f16 v89, v93, s59, v91 op_sel_hi:[1,0,1]
	v_pk_fma_f16 v7, v84, s59, v7 op_sel_hi:[1,0,1]
	v_and_b32_e32 v84, 0x7070707, v82
	v_and_b32_e32 v90, 0x7070707, v90
	v_perm_b32 v84, s2, v205, v84
	v_perm_b32 v90, s2, v205, v90
	v_lshlrev_b32_e32 v91, 4, v82
	v_and_or_b32 v84, v91, s4, v84
	v_and_or_b32 v82, v82, s4, v90
	v_perm_b32 v91, v82, v84, s33
	v_perm_b32 v92, v82, v84, s0
	v_perm_b32 v90, v82, v84, s5
	v_perm_b32 v82, v82, v84, s1
	v_pk_fma_f16 v84, v91, s60, v86 op_sel_hi:[1,0,1]
	v_pk_fma_f16 v86, v92, s60, v88 op_sel_hi:[1,0,1]
	v_lshrrev_b32_e32 v88, 4, v83
	v_pk_fma_f16 v8, v82, s60, v8 op_sel_hi:[1,0,1]
	v_and_b32_e32 v82, 0x7070707, v83
	v_and_b32_e32 v88, 0x7070707, v88
	v_pk_fma_f16 v9, v90, s60, v9 op_sel_hi:[1,0,1]
	v_perm_b32 v82, s2, v205, v82
	v_perm_b32 v88, s2, v205, v88
	v_lshlrev_b32_e32 v90, 4, v83
	v_and_or_b32 v82, v90, s4, v82
	v_and_or_b32 v83, v83, s4, v88
	v_perm_b32 v88, v83, v82, s5
	v_perm_b32 v90, v83, v82, s33
	v_perm_b32 v91, v83, v82, s0
	v_perm_b32 v82, v83, v82, s1
	v_pk_fma_f16 v83, v88, s60, v85 op_sel_hi:[1,0,1]
	v_readlane_b32 s36, v120, 24
	v_lshrrev_b32_e32 v88, 4, v80
	v_pk_fma_f16 v85, v90, s60, v87 op_sel_hi:[1,0,1]
	v_pk_fma_f16 v87, v91, s60, v89 op_sel_hi:[1,0,1]
	v_pk_fma_f16 v7, v82, s60, v7 op_sel_hi:[1,0,1]
	v_and_b32_e32 v82, 0x7070707, v80
	v_and_b32_e32 v88, 0x7070707, v88
	v_perm_b32 v82, s2, v205, v82
	v_perm_b32 v88, s2, v205, v88
	v_lshlrev_b32_e32 v89, 4, v80
	v_and_or_b32 v82, v89, s4, v82
	v_and_or_b32 v80, v80, s4, v88
	v_perm_b32 v89, v80, v82, s33
	v_perm_b32 v90, v80, v82, s0
	v_perm_b32 v88, v80, v82, s5
	v_perm_b32 v80, v80, v82, s1
	v_pk_fma_f16 v82, v89, s36, v84 op_sel_hi:[1,0,1]
	v_pk_fma_f16 v84, v90, s36, v86 op_sel_hi:[1,0,1]
	v_lshrrev_b32_e32 v86, 4, v81
	v_pk_fma_f16 v8, v80, s36, v8 op_sel_hi:[1,0,1]
	v_and_b32_e32 v80, 0x7070707, v81
	v_and_b32_e32 v86, 0x7070707, v86
	v_pk_fma_f16 v9, v88, s36, v9 op_sel_hi:[1,0,1]
	v_perm_b32 v80, s2, v205, v80
	v_perm_b32 v86, s2, v205, v86
	v_lshlrev_b32_e32 v88, 4, v81
	v_and_or_b32 v80, v88, s4, v80
	v_and_or_b32 v81, v81, s4, v86
	v_perm_b32 v86, v81, v80, s5
	v_perm_b32 v88, v81, v80, s33
	v_perm_b32 v89, v81, v80, s0
	v_perm_b32 v80, v81, v80, s1
	v_pk_fma_f16 v81, v86, s36, v83 op_sel_hi:[1,0,1]
	v_readlane_b32 s59, v120, 28
	v_lshrrev_b32_e32 v86, 4, v78
	v_pk_fma_f16 v83, v88, s36, v85 op_sel_hi:[1,0,1]
	v_pk_fma_f16 v85, v89, s36, v87 op_sel_hi:[1,0,1]
	v_pk_fma_f16 v7, v80, s36, v7 op_sel_hi:[1,0,1]
	v_and_b32_e32 v80, 0x7070707, v78
	v_and_b32_e32 v86, 0x7070707, v86
	v_perm_b32 v80, s2, v205, v80
	v_perm_b32 v86, s2, v205, v86
	v_lshlrev_b32_e32 v87, 4, v78
	v_and_or_b32 v80, v87, s4, v80
	v_and_or_b32 v78, v78, s4, v86
	v_perm_b32 v87, v78, v80, s33
	v_perm_b32 v88, v78, v80, s0
	v_perm_b32 v86, v78, v80, s5
	v_perm_b32 v78, v78, v80, s1
	v_pk_fma_f16 v80, v87, s59, v82 op_sel_hi:[1,0,1]
	v_pk_fma_f16 v82, v88, s59, v84 op_sel_hi:[1,0,1]
	v_lshrrev_b32_e32 v84, 4, v79
	v_pk_fma_f16 v8, v78, s59, v8 op_sel_hi:[1,0,1]
	v_and_b32_e32 v78, 0x7070707, v79
	v_and_b32_e32 v84, 0x7070707, v84
	v_pk_fma_f16 v9, v86, s59, v9 op_sel_hi:[1,0,1]
	v_perm_b32 v78, s2, v205, v78
	v_perm_b32 v84, s2, v205, v84
	v_lshlrev_b32_e32 v86, 4, v79
	v_and_or_b32 v78, v86, s4, v78
	v_and_or_b32 v79, v79, s4, v84
	v_perm_b32 v84, v79, v78, s5
	v_perm_b32 v86, v79, v78, s33
	v_perm_b32 v87, v79, v78, s0
	v_perm_b32 v78, v79, v78, s1
	v_pk_fma_f16 v79, v84, s59, v81 op_sel_hi:[1,0,1]
	v_readlane_b32 s60, v120, 32
	v_lshrrev_b32_e32 v84, 4, v76
	v_pk_fma_f16 v81, v86, s59, v83 op_sel_hi:[1,0,1]
	v_pk_fma_f16 v83, v87, s59, v85 op_sel_hi:[1,0,1]
	v_pk_fma_f16 v7, v78, s59, v7 op_sel_hi:[1,0,1]
	v_and_b32_e32 v78, 0x7070707, v76
	v_and_b32_e32 v84, 0x7070707, v84
	v_perm_b32 v78, s2, v205, v78
	v_perm_b32 v84, s2, v205, v84
	v_lshlrev_b32_e32 v85, 4, v76
	v_and_or_b32 v78, v85, s4, v78
	v_and_or_b32 v76, v76, s4, v84
	v_perm_b32 v85, v76, v78, s33
	v_perm_b32 v86, v76, v78, s0
	v_perm_b32 v84, v76, v78, s5
	v_perm_b32 v76, v76, v78, s1
	v_pk_fma_f16 v78, v85, s60, v80 op_sel_hi:[1,0,1]
	v_pk_fma_f16 v80, v86, s60, v82 op_sel_hi:[1,0,1]
	v_lshrrev_b32_e32 v82, 4, v77
	v_pk_fma_f16 v8, v76, s60, v8 op_sel_hi:[1,0,1]
	v_and_b32_e32 v76, 0x7070707, v77
	v_and_b32_e32 v82, 0x7070707, v82
	v_pk_fma_f16 v9, v84, s60, v9 op_sel_hi:[1,0,1]
	v_perm_b32 v76, s2, v205, v76
	v_perm_b32 v82, s2, v205, v82
	v_lshlrev_b32_e32 v84, 4, v77
	v_and_or_b32 v76, v84, s4, v76
	v_and_or_b32 v77, v77, s4, v82
	v_perm_b32 v82, v77, v76, s5
	v_perm_b32 v84, v77, v76, s33
	v_perm_b32 v85, v77, v76, s0
	v_perm_b32 v76, v77, v76, s1
	v_pk_fma_f16 v77, v82, s60, v79 op_sel_hi:[1,0,1]
	v_readlane_b32 s36, v120, 36
	v_lshrrev_b32_e32 v82, 4, v70
	v_pk_fma_f16 v79, v84, s60, v81 op_sel_hi:[1,0,1]
	v_pk_fma_f16 v81, v85, s60, v83 op_sel_hi:[1,0,1]
	v_pk_fma_f16 v7, v76, s60, v7 op_sel_hi:[1,0,1]
	v_and_b32_e32 v76, 0x7070707, v70
	v_and_b32_e32 v82, 0x7070707, v82
	v_perm_b32 v76, s2, v205, v76
	v_perm_b32 v82, s2, v205, v82
	v_lshlrev_b32_e32 v83, 4, v70
	v_and_or_b32 v76, v83, s4, v76
	v_and_or_b32 v70, v70, s4, v82
	v_perm_b32 v83, v70, v76, s33
	v_perm_b32 v84, v70, v76, s0
	v_perm_b32 v82, v70, v76, s5
	v_perm_b32 v70, v70, v76, s1
	v_pk_fma_f16 v76, v83, s36, v78 op_sel_hi:[1,0,1]
	v_pk_fma_f16 v78, v84, s36, v80 op_sel_hi:[1,0,1]
	v_lshrrev_b32_e32 v80, 4, v71
	v_pk_fma_f16 v8, v70, s36, v8 op_sel_hi:[1,0,1]
	v_and_b32_e32 v70, 0x7070707, v71
	v_and_b32_e32 v80, 0x7070707, v80
	v_pk_fma_f16 v9, v82, s36, v9 op_sel_hi:[1,0,1]
	v_perm_b32 v70, s2, v205, v70
	v_perm_b32 v80, s2, v205, v80
	v_lshlrev_b32_e32 v82, 4, v71
	v_and_or_b32 v70, v82, s4, v70
	v_and_or_b32 v71, v71, s4, v80
	v_perm_b32 v80, v71, v70, s5
	v_perm_b32 v82, v71, v70, s33
	v_perm_b32 v83, v71, v70, s0
	v_perm_b32 v70, v71, v70, s1
	v_pk_fma_f16 v71, v80, s36, v77 op_sel_hi:[1,0,1]
	v_readlane_b32 s59, v120, 40
	v_lshrrev_b32_e32 v80, 4, v66
	v_pk_fma_f16 v77, v82, s36, v79 op_sel_hi:[1,0,1]
	v_pk_fma_f16 v79, v83, s36, v81 op_sel_hi:[1,0,1]
	v_pk_fma_f16 v7, v70, s36, v7 op_sel_hi:[1,0,1]
	v_and_b32_e32 v70, 0x7070707, v66
	v_and_b32_e32 v80, 0x7070707, v80
	v_perm_b32 v70, s2, v205, v70
	v_perm_b32 v80, s2, v205, v80
	v_lshlrev_b32_e32 v81, 4, v66
	v_and_or_b32 v70, v81, s4, v70
	v_and_or_b32 v66, v66, s4, v80
	v_perm_b32 v81, v66, v70, s33
	v_perm_b32 v82, v66, v70, s0
	v_perm_b32 v80, v66, v70, s5
	v_perm_b32 v66, v66, v70, s1
	v_pk_fma_f16 v70, v81, s59, v76 op_sel_hi:[1,0,1]
	v_pk_fma_f16 v76, v82, s59, v78 op_sel_hi:[1,0,1]
	v_lshrrev_b32_e32 v78, 4, v67
	v_pk_fma_f16 v8, v66, s59, v8 op_sel_hi:[1,0,1]
	v_and_b32_e32 v66, 0x7070707, v67
	v_and_b32_e32 v78, 0x7070707, v78
	v_pk_fma_f16 v9, v80, s59, v9 op_sel_hi:[1,0,1]
	v_perm_b32 v66, s2, v205, v66
	v_perm_b32 v78, s2, v205, v78
	v_lshlrev_b32_e32 v80, 4, v67
	v_and_or_b32 v66, v80, s4, v66
	v_and_or_b32 v67, v67, s4, v78
	v_perm_b32 v78, v67, v66, s5
	v_perm_b32 v80, v67, v66, s33
	v_perm_b32 v81, v67, v66, s0
	v_perm_b32 v66, v67, v66, s1
	v_pk_fma_f16 v67, v78, s59, v71 op_sel_hi:[1,0,1]
	v_readlane_b32 s60, v120, 44
	v_lshrrev_b32_e32 v78, 4, v72
	v_pk_fma_f16 v71, v80, s59, v77 op_sel_hi:[1,0,1]
	v_pk_fma_f16 v77, v81, s59, v79 op_sel_hi:[1,0,1]
	v_pk_fma_f16 v7, v66, s59, v7 op_sel_hi:[1,0,1]
	v_and_b32_e32 v66, 0x7070707, v72
	v_and_b32_e32 v78, 0x7070707, v78
	v_perm_b32 v66, s2, v205, v66
	v_perm_b32 v78, s2, v205, v78
	v_lshlrev_b32_e32 v79, 4, v72
	v_and_or_b32 v66, v79, s4, v66
	v_and_or_b32 v72, v72, s4, v78
	v_perm_b32 v80, v72, v66, s0
	v_perm_b32 v78, v72, v66, s5
	v_perm_b32 v79, v72, v66, s33
	v_perm_b32 v66, v72, v66, s1
	v_pk_fma_f16 v72, v80, s60, v76 op_sel_hi:[1,0,1]
	v_lshrrev_b32_e32 v76, 4, v73
	v_pk_fma_f16 v8, v66, s60, v8 op_sel_hi:[1,0,1]
	v_and_b32_e32 v66, 0x7070707, v73
	v_and_b32_e32 v76, 0x7070707, v76
	v_pk_fma_f16 v9, v78, s60, v9 op_sel_hi:[1,0,1]
	v_perm_b32 v66, s2, v205, v66
	v_perm_b32 v76, s2, v205, v76
	v_lshlrev_b32_e32 v78, 4, v73
	v_and_or_b32 v66, v78, s4, v66
	v_and_or_b32 v73, v73, s4, v76
	v_perm_b32 v76, v73, v66, s5
	v_pk_fma_f16 v70, v79, s60, v70 op_sel_hi:[1,0,1]
	v_perm_b32 v78, v73, v66, s33
	v_perm_b32 v79, v73, v66, s0
	v_perm_b32 v66, v73, v66, s1
	v_pk_fma_f16 v67, v76, s60, v67 op_sel_hi:[1,0,1]
	v_readlane_b32 s36, v120, 48
	v_lshrrev_b32_e32 v76, 4, v68
	v_pk_fma_f16 v71, v78, s60, v71 op_sel_hi:[1,0,1]
	v_pk_fma_f16 v73, v79, s60, v77 op_sel_hi:[1,0,1]
	v_pk_fma_f16 v7, v66, s60, v7 op_sel_hi:[1,0,1]
	v_and_b32_e32 v66, 0x7070707, v68
	v_and_b32_e32 v76, 0x7070707, v76
	v_perm_b32 v66, s2, v205, v66
	v_perm_b32 v76, s2, v205, v76
	v_lshlrev_b32_e32 v77, 4, v68
	v_and_or_b32 v66, v77, s4, v66
	v_and_or_b32 v68, v68, s4, v76
	v_perm_b32 v77, v68, v66, s33
	v_perm_b32 v78, v68, v66, s0
	v_perm_b32 v76, v68, v66, s5
	v_perm_b32 v66, v68, v66, s1
	v_pk_fma_f16 v68, v77, s36, v70 op_sel_hi:[1,0,1]
	v_pk_fma_f16 v70, v78, s36, v72 op_sel_hi:[1,0,1]
	v_lshrrev_b32_e32 v72, 4, v69
	v_pk_fma_f16 v8, v66, s36, v8 op_sel_hi:[1,0,1]
	v_and_b32_e32 v66, 0x7070707, v69
	v_and_b32_e32 v72, 0x7070707, v72
	v_pk_fma_f16 v9, v76, s36, v9 op_sel_hi:[1,0,1]
	v_perm_b32 v66, s2, v205, v66
	v_perm_b32 v72, s2, v205, v72
	v_lshlrev_b32_e32 v76, 4, v69
	v_and_or_b32 v66, v76, s4, v66
	v_and_or_b32 v69, v69, s4, v72
	v_perm_b32 v72, v69, v66, s5
	v_perm_b32 v76, v69, v66, s33
	v_perm_b32 v77, v69, v66, s0
	v_perm_b32 v66, v69, v66, s1
	v_pk_fma_f16 v67, v72, s36, v67 op_sel_hi:[1,0,1]
	v_readlane_b32 s59, v120, 52
	v_lshrrev_b32_e32 v72, 4, v64
	v_pk_fma_f16 v69, v76, s36, v71 op_sel_hi:[1,0,1]
	v_pk_fma_f16 v71, v77, s36, v73 op_sel_hi:[1,0,1]
	v_pk_fma_f16 v7, v66, s36, v7 op_sel_hi:[1,0,1]
	v_and_b32_e32 v66, 0x7070707, v64
	v_and_b32_e32 v72, 0x7070707, v72
	v_perm_b32 v66, s2, v205, v66
	v_perm_b32 v72, s2, v205, v72
	v_lshlrev_b32_e32 v73, 4, v64
	v_and_or_b32 v66, v73, s4, v66
	v_and_or_b32 v64, v64, s4, v72
	v_perm_b32 v73, v64, v66, s33
	v_perm_b32 v76, v64, v66, s0
	v_perm_b32 v72, v64, v66, s5
	v_perm_b32 v64, v64, v66, s1
	v_pk_fma_f16 v66, v73, s59, v68 op_sel_hi:[1,0,1]
	v_pk_fma_f16 v68, v76, s59, v70 op_sel_hi:[1,0,1]
	v_lshrrev_b32_e32 v70, 4, v65
	v_pk_fma_f16 v8, v64, s59, v8 op_sel_hi:[1,0,1]
	v_and_b32_e32 v64, 0x7070707, v65
	v_and_b32_e32 v70, 0x7070707, v70
	v_pk_fma_f16 v9, v72, s59, v9 op_sel_hi:[1,0,1]
	v_perm_b32 v64, s2, v205, v64
	v_perm_b32 v70, s2, v205, v70
	v_lshlrev_b32_e32 v72, 4, v65
	v_and_or_b32 v64, v72, s4, v64
	v_and_or_b32 v65, v65, s4, v70
	v_perm_b32 v70, v65, v64, s5
	v_perm_b32 v72, v65, v64, s33
	v_perm_b32 v73, v65, v64, s0
	v_perm_b32 v64, v65, v64, s1
	v_pk_fma_f16 v65, v70, s59, v67 op_sel_hi:[1,0,1]
	v_readlane_b32 s60, v120, 56
	v_lshrrev_b32_e32 v70, 4, v62
	v_pk_fma_f16 v67, v72, s59, v69 op_sel_hi:[1,0,1]
	v_pk_fma_f16 v69, v73, s59, v71 op_sel_hi:[1,0,1]
	v_pk_fma_f16 v7, v64, s59, v7 op_sel_hi:[1,0,1]
	v_and_b32_e32 v64, 0x7070707, v62
	v_and_b32_e32 v70, 0x7070707, v70
	v_perm_b32 v64, s2, v205, v64
	v_perm_b32 v70, s2, v205, v70
	v_lshlrev_b32_e32 v71, 4, v62
	v_and_or_b32 v64, v71, s4, v64
	v_and_or_b32 v62, v62, s4, v70
	v_perm_b32 v71, v62, v64, s33
	v_perm_b32 v72, v62, v64, s0
	v_perm_b32 v70, v62, v64, s5
	v_perm_b32 v62, v62, v64, s1
	v_pk_fma_f16 v64, v71, s60, v66 op_sel_hi:[1,0,1]
	v_pk_fma_f16 v66, v72, s60, v68 op_sel_hi:[1,0,1]
	v_lshrrev_b32_e32 v68, 4, v63
	v_pk_fma_f16 v8, v62, s60, v8 op_sel_hi:[1,0,1]
	v_and_b32_e32 v62, 0x7070707, v63
	v_and_b32_e32 v68, 0x7070707, v68
	v_pk_fma_f16 v9, v70, s60, v9 op_sel_hi:[1,0,1]
	v_perm_b32 v62, s2, v205, v62
	v_perm_b32 v68, s2, v205, v68
	v_lshlrev_b32_e32 v70, 4, v63
	v_and_or_b32 v62, v70, s4, v62
	v_and_or_b32 v63, v63, s4, v68
	v_perm_b32 v68, v63, v62, s5
	v_perm_b32 v70, v63, v62, s33
	v_perm_b32 v71, v63, v62, s0
	v_perm_b32 v62, v63, v62, s1
	v_pk_fma_f16 v7, v62, s60, v7 op_sel_hi:[1,0,1]
	v_readlane_b32 s36, v120, 60
	v_lshrrev_b32_e32 v62, 4, v50
	v_pk_fma_f16 v63, v68, s60, v65 op_sel_hi:[1,0,1]
	v_pk_fma_f16 v65, v70, s60, v67 op_sel_hi:[1,0,1]
	v_pk_fma_f16 v67, v71, s60, v69 op_sel_hi:[1,0,1]
	v_and_b32_e32 v15, 0x7070707, v50
	v_and_b32_e32 v62, 0x7070707, v62
	v_perm_b32 v15, s2, v205, v15
	v_perm_b32 v62, s2, v205, v62
	v_lshlrev_b32_e32 v68, 4, v50
	v_and_or_b32 v15, v68, s4, v15
	v_and_or_b32 v50, v50, s4, v62
	v_perm_b32 v62, v50, v15, s5
	v_perm_b32 v68, v50, v15, s33
	v_perm_b32 v69, v50, v15, s0
	v_perm_b32 v15, v50, v15, s1
	v_pk_fma_f16 v105, v62, s36, v9 op_sel_hi:[1,0,1]
	v_lshrrev_b32_e32 v9, 4, v51
	v_pk_fma_f16 v102, v15, s36, v8 op_sel_hi:[1,0,1]
	v_and_b32_e32 v8, 0x7070707, v51
	v_and_b32_e32 v9, 0x7070707, v9
	v_perm_b32 v8, s2, v205, v8
	v_perm_b32 v9, s2, v205, v9
	v_lshlrev_b32_e32 v15, 4, v51
	v_and_or_b32 v8, v15, s4, v8
	v_and_or_b32 v9, v51, s4, v9
	v_perm_b32 v15, v9, v8, s5
	v_perm_b32 v50, v9, v8, s33
	v_perm_b32 v51, v9, v8, s0
	v_perm_b32 v8, v9, v8, s1
	v_pk_fma_f16 v104, v68, s36, v64 op_sel_hi:[1,0,1]
	v_pk_fma_f16 v103, v69, s36, v66 op_sel_hi:[1,0,1]
	v_pk_fma_f16 v101, v15, s36, v63 op_sel_hi:[1,0,1]
	v_pk_fma_f16 v100, v50, s36, v65 op_sel_hi:[1,0,1]
	v_pk_fma_f16 v99, v51, s36, v67 op_sel_hi:[1,0,1]
	v_pk_fma_f16 v15, v8, s36, v7 op_sel_hi:[1,0,1]
	v_lshl_add_u64 v[6:7], v[18:19], 0, s[10:11]
	global_load_dwordx2 v[92:93], v[6:7], off
	v_lshl_add_u64 v[6:7], v[18:19], 0, s[12:13]
	global_load_dwordx2 v[90:91], v[6:7], off
	v_lshl_add_u64 v[6:7], v[18:19], 0, s[14:15]
	global_load_dwordx2 v[88:89], v[6:7], off
	v_lshl_add_u64 v[6:7], v[18:19], 0, s[16:17]
	global_load_dwordx2 v[86:87], v[6:7], off
	v_lshl_add_u64 v[6:7], v[18:19], 0, s[18:19]
	global_load_dwordx2 v[84:85], v[6:7], off
	v_lshl_add_u64 v[6:7], v[18:19], 0, s[20:21]
	global_load_dwordx2 v[82:83], v[6:7], off
	v_lshl_add_u64 v[6:7], v[18:19], 0, s[22:23]
	global_load_dwordx2 v[80:81], v[6:7], off
	v_lshl_add_u64 v[6:7], v[18:19], 0, s[24:25]
	global_load_dwordx2 v[78:79], v[6:7], off
	v_lshl_add_u64 v[6:7], v[18:19], 0, s[26:27]
	global_load_dwordx2 v[76:77], v[6:7], off
	v_lshl_add_u64 v[6:7], v[18:19], 0, s[28:29]
	v_readlane_b32 s50, v96, 13
	global_load_dwordx2 v[70:71], v[6:7], off
	v_lshl_add_u64 v[6:7], v[18:19], 0, s[30:31]
	global_load_dwordx2 v[40:41], v[40:41], off
	v_lshl_add_u64 v[52:53], v[16:17], 0, s[34:35]
	s_lshl_b64 s[38:39], s[38:39], 9
	s_ashr_i32 s51, s50, 31
	v_readlane_b32 s52, v96, 14
	global_load_dwordx2 v[66:67], v[6:7], off
	v_lshl_add_u64 v[6:7], v[18:19], 0, s[34:35]
	global_load_dwordx2 v[60:61], v[52:53], off
	global_load_dwordx2 v[72:73], v[6:7], off
	v_lshl_add_u64 v[52:53], v[16:17], 0, s[38:39]
	s_lshl_b64 s[50:51], s[50:51], 9
	s_ashr_i32 s53, s52, 31
	v_readlane_b32 s54, v96, 15
	v_lshl_add_u64 v[6:7], v[18:19], 0, s[38:39]
	global_load_dwordx2 v[58:59], v[52:53], off
	global_load_dwordx2 v[68:69], v[6:7], off
	v_lshl_add_u64 v[52:53], v[16:17], 0, s[50:51]
	s_lshl_b64 s[52:53], s[52:53], 9
	s_ashr_i32 s55, s54, 31
	v_lshl_add_u64 v[6:7], v[18:19], 0, s[50:51]
	global_load_dwordx2 v[56:57], v[52:53], off
	global_load_dwordx2 v[64:65], v[6:7], off
	v_lshl_add_u64 v[52:53], v[16:17], 0, s[52:53]
	s_lshl_b64 s[54:55], s[54:55], 9
	v_lshl_add_u64 v[6:7], v[18:19], 0, s[52:53]
	global_load_dwordx2 v[54:55], v[52:53], off
	global_load_dwordx2 v[62:63], v[6:7], off
	v_lshl_add_u64 v[52:53], v[16:17], 0, s[54:55]
	v_lshl_add_u64 v[6:7], v[18:19], 0, s[54:55]
	global_load_dwordx2 v[52:53], v[52:53], off
	s_cmpk_eq_i32 s56, 0x90
	global_load_dwordx2 v[50:51], v[6:7], off
	s_cbranch_scc0 .LBB0_770
	v_lshl_add_u64 v[94:95], v[2:3], 2, v[44:45]
	v_mov_b32_e32 v106, v208
	v_mov_b32_e32 v107, v209
	v_mov_b32_e32 v108, v210
	v_mov_b32_e32 v109, v211
	v_mov_b32_e32 v8, v212
	v_mov_b32_e32 v9, v213
	v_mov_b32_e32 v10, v214
	v_mov_b32_e32 v11, v215
	v_mov_b32_e32 v4, v216
	v_mov_b32_e32 v5, v217
	v_mov_b32_e32 v6, v218
	v_mov_b32_e32 v7, v219
	v_mov_b32_e32 v0, v220
	v_mov_b32_e32 v1, v221
	v_mov_b32_e32 v2, v222
	v_mov_b32_e32 v3, v223
	v_cvt_f32_f16_sdwa v13, v105 dst_sel:DWORD dst_unused:UNUSED_PAD src0_sel:WORD_1
	v_cvt_f32_f16_e32 v12, v105
	s_mov_b32 s12, 0x800000
	v_readlane_b32 s10, v255, 5
	v_readlane_b32 s11, v255, 6
	v_pk_add_f32 v[0:1], v[0:1], v[12:13]
	v_cvt_f32_f16_sdwa v13, v104 dst_sel:DWORD dst_unused:UNUSED_PAD src0_sel:WORD_1
	v_cvt_f32_f16_e32 v12, v104
	v_lshl_add_u64 v[48:49], v[48:49], 0, s[10:11]
	v_pk_add_f32 v[2:3], v[2:3], v[12:13]
	v_cvt_f32_f16_sdwa v13, v103 dst_sel:DWORD dst_unused:UNUSED_PAD src0_sel:WORD_1
	v_cvt_f32_f16_e32 v12, v103
	global_store_dwordx4 v[94:95], v[0:3], off
	v_pk_add_f32 v[4:5], v[4:5], v[12:13]
	v_cvt_f32_f16_sdwa v13, v102 dst_sel:DWORD dst_unused:UNUSED_PAD src0_sel:WORD_1
	v_cvt_f32_f16_e32 v12, v102
	v_mov_b32_e32 v102, v1
	v_mov_b32_e32 v103, v5
	v_pk_mul_f32 v[102:103], v[102:103], v[102:103]
	v_pk_add_f32 v[6:7], v[6:7], v[12:13]
	v_mov_b32_e32 v12, v0
	v_mov_b32_e32 v13, v4
	v_pk_fma_f32 v[12:13], v[12:13], v[12:13], v[102:103]
	v_mov_b32_e32 v102, v2
	v_mov_b32_e32 v103, v6
	v_pk_fma_f32 v[12:13], v[102:103], v[102:103], v[12:13]
	v_mov_b32_e32 v102, v3
	v_mov_b32_e32 v103, v7
	v_pk_fma_f32 v[102:103], v[102:103], v[102:103], v[12:13]
	v_cvt_f32_f16_sdwa v13, v101 dst_sel:DWORD dst_unused:UNUSED_PAD src0_sel:WORD_1
	v_cvt_f32_f16_e32 v12, v101
	v_cvt_f32_f16_sdwa v101, v15 dst_sel:DWORD dst_unused:UNUSED_PAD src0_sel:WORD_1
	global_store_dwordx4 v[94:95], v[4:7], off offset:16
	v_pk_add_f32 v[8:9], v[8:9], v[12:13]
	v_cvt_f32_f16_sdwa v13, v100 dst_sel:DWORD dst_unused:UNUSED_PAD src0_sel:WORD_1
	v_cvt_f32_f16_e32 v12, v100
	v_cvt_f32_f16_e32 v100, v15
	v_pk_add_f32 v[10:11], v[10:11], v[12:13]
	v_cvt_f32_f16_sdwa v13, v99 dst_sel:DWORD dst_unused:UNUSED_PAD src0_sel:WORD_1
	v_cvt_f32_f16_e32 v12, v99
	v_pk_add_f32 v[14:15], v[108:109], v[100:101]
	v_mov_b32_e32 v100, v9
	global_store_dwordx4 v[94:95], v[8:11], off offset:32
	v_pk_add_f32 v[12:13], v[106:107], v[12:13]
	global_store_dwordx4 v[94:95], v[12:15], off offset:48
	v_mov_b32_e32 v101, v13
	v_mov_b32_e32 v94, v8
	v_mov_b32_e32 v95, v12
	v_pk_mul_f32 v[100:101], v[100:101], v[100:101]
	v_add_f32_e32 v99, v102, v103
	v_pk_fma_f32 v[94:95], v[94:95], v[94:95], v[100:101]
	v_mov_b32_e32 v100, v10
	v_mov_b32_e32 v101, v14
	v_pk_fma_f32 v[94:95], v[100:101], v[100:101], v[94:95]
	v_mov_b32_e32 v100, v11
	v_mov_b32_e32 v101, v15
	v_pk_fma_f32 v[94:95], v[100:101], v[100:101], v[94:95]
	global_load_dwordx4 v[100:103], v[46:47], off offset:48
	global_load_dwordx4 v[104:107], v[46:47], off offset:32
	global_load_dwordx4 v[108:111], v[46:47], off offset:16
	global_load_dwordx4 v[112:115], v[46:47], off
	v_add_f32_e32 v94, v99, v94
	v_add_f32_e32 v94, v94, v95
	ds_bpermute_b32 v95, v184, v94
	s_waitcnt lgkmcnt(0)
	v_add_f32_e32 v94, v94, v95
	ds_bpermute_b32 v95, v185, v94
	s_waitcnt lgkmcnt(0)
	v_add_f32_e32 v94, v94, v95
	ds_bpermute_b32 v95, v186, v94
	s_waitcnt lgkmcnt(0)
	v_add_f32_e32 v94, v94, v95
	ds_bpermute_b32 v95, v187, v94
	s_waitcnt lgkmcnt(0)
	v_add_f32_e32 v94, v94, v95
	ds_bpermute_b32 v95, v188, v94
	s_waitcnt lgkmcnt(0)
	v_add_f32_e32 v94, v94, v95
	ds_bpermute_b32 v95, v189, v94
	s_waitcnt lgkmcnt(0)
	v_add_f32_e32 v94, v94, v95
	v_fmamk_f32 v94, v94, 0x3a800000, v191
	v_cmp_gt_f32_e32 vcc, s12, v94
	v_mul_f32_e32 v95, 0x4b800000, v94
	s_nop 0
	v_cndmask_b32_e32 v94, v94, v95, vcc
	v_rsq_f32_e32 v94, v94
	s_nop 0
	v_mul_f32_e32 v95, 0x45800000, v94
	v_cndmask_b32_e32 v94, v94, v95, vcc
	v_pk_mul_f32 v[0:1], v[0:1], v[94:95] op_sel_hi:[1,0]
	v_pk_mul_f32 v[2:3], v[2:3], v[94:95] op_sel_hi:[1,0]
	s_waitcnt vmcnt(0)
	v_pk_mul_f32 v[0:1], v[112:113], v[0:1]
	v_pk_mul_f32 v[2:3], v[114:115], v[2:3]
	v_cvt_pk_bf16_f32 v0, v0, v1
	v_cvt_pk_bf16_f32 v1, v2, v3
	v_pk_mul_f32 v[2:3], v[4:5], v[94:95] op_sel_hi:[1,0]
	v_pk_mul_f32 v[4:5], v[6:7], v[94:95] op_sel_hi:[1,0]
	v_pk_mul_f32 v[2:3], v[108:109], v[2:3]
	v_pk_mul_f32 v[4:5], v[110:111], v[4:5]
	v_cvt_pk_bf16_f32 v2, v2, v3
	v_cvt_pk_bf16_f32 v3, v4, v5
	v_pk_mul_f32 v[4:5], v[8:9], v[94:95] op_sel_hi:[1,0]
	v_pk_mul_f32 v[6:7], v[10:11], v[94:95] op_sel_hi:[1,0]
	v_pk_mul_f32 v[4:5], v[104:105], v[4:5]
	v_pk_mul_f32 v[6:7], v[6:7], v[106:107]
	v_cvt_pk_bf16_f32 v4, v4, v5
	v_cvt_pk_bf16_f32 v5, v6, v7
	v_pk_mul_f32 v[6:7], v[12:13], v[94:95] op_sel_hi:[1,0]
	v_pk_mul_f32 v[8:9], v[14:15], v[94:95] op_sel_hi:[1,0]
	v_pk_mul_f32 v[6:7], v[6:7], v[100:101]
	v_pk_mul_f32 v[8:9], v[8:9], v[102:103]
	v_cvt_pk_bf16_f32 v6, v6, v7
	v_cvt_pk_bf16_f32 v7, v8, v9
	global_store_dwordx4 v[74:75], v[0:3], off
	global_store_dwordx4 v[74:75], v[4:7], off offset:16
	s_nop 0
	v_mov_b32_e32 v0, v98
	s_andn2_b64 exec, exec, s[8:9]
	s_cbranch_execnz .LBB0_769
